# s28
# speedup vs baseline: 1.0127x; 1.0127x over previous
.LBB1_5:
	v_lshlrev_b32_e32 v67, 4, v1
	v_lshrrev_b32_e32 v1, 1, v1
	v_lshrrev_b32_e32 v69, 5, v132
	v_ashrrev_i32_e32 v66, 4, v132
	v_bitop3_b32 v1, v1, v69, 7 bitop3:0x78
	s_add_u32 s22, s24, s2
	v_lshlrev_b32_e32 v68, 7, v66
	v_lshlrev_b32_e32 v1, 4, v1
	v_and_b32_e32 v0, 8, v0
	s_addc_u32 s90, s25, s3
	v_lshl_or_b32 v201, v66, 12, v67
	v_or3_b32 v0, v68, v1, v0
	v_add_u32_e32 v100, 0x10000, v0
	v_cvt_pk_f16_f32 v1, v64, v65
	v_cvt_pk_f16_f32 v0, v62, v63
	v_cvt_pk_f16_f32 v61, v60, v61
	v_cvt_pk_f16_f32 v60, v58, v59
	ds_write2st64_b64 v100, v[0:1], v[60:61] offset1:8
	v_cvt_pk_f16_f32 v1, v56, v57
	v_cvt_pk_f16_f32 v0, v54, v55
	v_cvt_pk_f16_f32 v53, v52, v53
	v_cvt_pk_f16_f32 v52, v50, v51
	ds_write2st64_b64 v100, v[0:1], v[52:53] offset0:16 offset1:24
	v_cvt_pk_f16_f32 v1, v48, v49
	v_cvt_pk_f16_f32 v0, v46, v47
	v_cvt_pk_f16_f32 v45, v44, v45
	v_cvt_pk_f16_f32 v44, v42, v43
	ds_write2st64_b64 v100, v[0:1], v[44:45] offset0:32 offset1:40
	v_cvt_pk_f16_f32 v1, v40, v41
	v_cvt_pk_f16_f32 v0, v38, v39
	v_cvt_pk_f16_f32 v37, v36, v37
	v_cvt_pk_f16_f32 v36, v34, v35
	ds_write2st64_b64 v100, v[0:1], v[36:37] offset0:48 offset1:56
	s_add_u32 s0, s22, 0x200
	s_addc_u32 s1, s90, 0
	s_add_u32 s70, s0, 0x20000
	s_addc_u32 s71, s1, 0
	s_add_u32 s72, s0, 0x40000
	s_addc_u32 s73, s1, 0
	s_add_u32 s92, s0, 0x60000
	s_addc_u32 s93, s1, 0
	s_add_u32 s94, s0, 0x80000
	s_addc_u32 s95, s1, 0
	s_add_u32 s96, s0, 0xa0000
	s_addc_u32 s97, s1, 0
	s_add_u32 s98, s0, 0xc0000
	s_addc_u32 s99, s1, 0
	s_add_u32 s80, s0, 0xe0000
	s_addc_u32 s81, s1, 0
	global_load_dwordx4 v[70:73], v201, s[0:1] nt
	global_load_dwordx4 v[42:45], v201, s[70:71] nt
	global_load_dwordx4 v[46:49], v201, s[72:73] nt
	global_load_dwordx4 v[66:69], v201, s[92:93] nt
	global_load_dwordx4 v[62:65], v201, s[94:95] nt
	global_load_dwordx4 v[58:61], v201, s[96:97] nt
	global_load_dwordx4 v[54:57], v201, s[98:99] nt
	global_load_dwordx4 v[50:53], v201, s[80:81] nt
	s_waitcnt vmcnt(8)
	s_waitcnt lgkmcnt(0)
	s_barrier
	ds_read_b128 v[34:37], v131
	ds_read_b128 v[38:41], v131 offset:2048
	ds_read_b128 v[74:77], v131 offset:4096
	ds_read_b128 v[78:81], v131 offset:6144
	ds_read_b128 v[82:85], v129
	ds_read_b128 v[86:89], v129 offset:2048
	s_add_u32 s70, s22, 0x300
	v_add_u32_e32 v95, 0x8000, v94
	v_lshl_add_u64 v[0:1], s[26:27], 0, v[196:197]
	s_addc_u32 s71, s90, 0
	v_readfirstlane_b32 s0, v95
	s_mov_b32 m0, s0
	v_cvt_pk_f16_f32 v33, v32, v33
	global_load_lds_dwordx4 v[0:1], off
	v_cvt_pk_f16_f32 v32, v30, v31
	ds_write_b64 v100, v[32:33] offset:32768
	s_setprio 1
	s_waitcnt lgkmcnt(1)
	v_mfma_f32_16x16x32_f16 v[90:93], v[82:85], v[34:37], 0
	v_mfma_f32_16x16x32_f16 v[102:105], v[82:85], v[38:41], 0
	v_mfma_f32_16x16x32_f16 v[106:109], v[82:85], v[74:77], 0
	v_mfma_f32_16x16x32_f16 v[82:85], v[82:85], v[78:81], 0
	v_mfma_f32_16x16x32_f16 v[110:113], v[86:89], v[34:37], 0
	v_mfma_f32_16x16x32_f16 v[114:117], v[86:89], v[38:41], 0
	v_mfma_f32_16x16x32_f16 v[118:121], v[86:89], v[74:77], 0
	v_mfma_f32_16x16x32_f16 v[86:89], v[86:89], v[78:81], 0
	s_setprio 0
	ds_read_b128 v[122:125], v129 offset:4096
	ds_read_b128 v[134:137], v129 offset:6144
	v_add_u32_e32 v96, 0xa000, v94
	v_lshl_add_u64 v[98:99], v[0:1], 0, s[58:59]
	v_readfirstlane_b32 s1, v96
	s_mov_b32 m0, s1
	v_cvt_pk_f16_f32 v29, v28, v29
	global_load_lds_dwordx4 v[98:99], off
	v_cvt_pk_f16_f32 v28, v26, v27
	ds_write_b64 v100, v[28:29] offset:36864
	s_add_u32 s70, s22, 0x20300
	s_addc_u32 s71, s90, 0
	s_add_u32 s100, s22, 0x300
	s_addc_u32 s101, s90, 0
	global_load_dwordx4 v[30:33], v201, s[100:101] nt
	s_setprio 1
	s_waitcnt lgkmcnt(1)
	v_mfma_f32_16x16x32_f16 v[138:141], v[122:125], v[34:37], 0
	v_mfma_f32_16x16x32_f16 v[142:145], v[122:125], v[38:41], 0
	v_mfma_f32_16x16x32_f16 v[146:149], v[122:125], v[74:77], 0
	v_mfma_f32_16x16x32_f16 v[122:125], v[122:125], v[78:81], 0
	v_mfma_f32_16x16x32_f16 v[150:153], v[134:137], v[34:37], 0
	v_mfma_f32_16x16x32_f16 v[154:157], v[134:137], v[38:41], 0
	v_mfma_f32_16x16x32_f16 v[158:161], v[134:137], v[74:77], 0
	v_mfma_f32_16x16x32_f16 v[134:137], v[134:137], v[78:81], 0
	s_setprio 0
	ds_read_b128 v[162:165], v129 offset:8192
	ds_read_b128 v[166:169], v129 offset:10240
	v_add_u32_e32 v97, 0xc000, v94
	v_lshl_add_u64 v[98:99], v[0:1], 0, s[60:61]
	v_readfirstlane_b32 s71, v97
	s_mov_b32 m0, s71
	v_cvt_pk_f16_f32 v25, v24, v25
	global_load_lds_dwordx4 v[98:99], off
	v_cvt_pk_f16_f32 v24, v22, v23
	ds_write_b64 v100, v[24:25] offset:40960
	s_add_u32 s72, s22, 0x40300
	s_addc_u32 s73, s90, 0
	s_add_u32 s100, s22, 0x20300
	s_addc_u32 s101, s90, 0
	global_load_dwordx4 v[26:29], v201, s[100:101] nt
	s_setprio 1
	s_waitcnt lgkmcnt(1)
	v_mfma_f32_16x16x32_f16 v[170:173], v[162:165], v[34:37], 0
	v_mfma_f32_16x16x32_f16 v[174:177], v[162:165], v[38:41], 0
	v_mfma_f32_16x16x32_f16 v[178:181], v[162:165], v[74:77], 0
	v_mfma_f32_16x16x32_f16 v[162:165], v[162:165], v[78:81], 0
	v_mfma_f32_16x16x32_f16 v[182:185], v[166:169], v[34:37], 0
	v_mfma_f32_16x16x32_f16 v[186:189], v[166:169], v[38:41], 0
	v_mfma_f32_16x16x32_f16 v[190:193], v[166:169], v[74:77], 0
	v_mfma_f32_16x16x32_f16 v[166:169], v[166:169], v[78:81], 0
	s_setprio 0
	ds_read_b128 v[202:205], v129 offset:12288
	ds_read_b128 v[206:209], v129 offset:14336
	v_add_u32_e32 v98, 0xe000, v94
	v_lshl_add_u64 v[0:1], v[0:1], 0, s[62:63]
	v_readfirstlane_b32 s72, v98
	s_mov_b32 m0, s72
	s_nop 0
	global_load_lds_dwordx4 v[0:1], off
	v_cvt_pk_f16_f32 v1, v20, v21
	v_cvt_pk_f16_f32 v0, v18, v19
	ds_write_b64 v100, v[0:1] offset:45056
	s_add_u32 s80, s22, 0x60300
	s_addc_u32 s81, s90, 0
	s_add_u32 s100, s22, 0x40300
	s_addc_u32 s101, s90, 0
	global_load_dwordx4 v[22:25], v201, s[100:101] nt
	s_setprio 1
	s_waitcnt lgkmcnt(1)
	v_mfma_f32_16x16x32_f16 v[210:213], v[202:205], v[34:37], 0
	v_mfma_f32_16x16x32_f16 v[214:217], v[202:205], v[38:41], 0
	v_mfma_f32_16x16x32_f16 v[218:221], v[202:205], v[74:77], 0
	v_mfma_f32_16x16x32_f16 v[202:205], v[202:205], v[78:81], 0
	v_mfma_f32_16x16x32_f16 v[74:77], v[206:209], v[74:77], 0
	v_mfma_f32_16x16x32_f16 v[78:81], v[206:209], v[78:81], 0
	v_mfma_f32_16x16x32_f16 v[222:225], v[206:209], v[34:37], 0
	v_mfma_f32_16x16x32_f16 v[226:229], v[206:209], v[38:41], 0
	s_setprio 0
	ds_read_b128 v[206:209], v128
	ds_read_b128 v[230:233], v128 offset:2048
	ds_read_b128 v[234:237], v128 offset:4096
	ds_read_b128 v[238:241], v128 offset:6144
	ds_read_b128 v[34:37], v130
	ds_read_b128 v[38:41], v130 offset:2048
	v_cvt_pk_f16_f32 v1, v16, v17
	v_cvt_pk_f16_f32 v0, v14, v15
	ds_write_b64 v100, v[0:1] offset:49152
	s_add_u32 s80, s22, 0x80300
	s_addc_u32 s81, s90, 0
	s_add_u32 s100, s22, 0x60300
	s_addc_u32 s101, s90, 0
	global_load_dwordx4 v[18:21], v201, s[100:101] nt
	s_setprio 1
	s_waitcnt lgkmcnt(1)
	v_mfma_f32_16x16x32_f16 v[90:93], v[34:37], v[206:209], v[90:93]
	v_mfma_f32_16x16x32_f16 v[102:105], v[34:37], v[230:233], v[102:105]
	v_mfma_f32_16x16x32_f16 v[106:109], v[34:37], v[234:237], v[106:109]
	v_mfma_f32_16x16x32_f16 v[82:85], v[34:37], v[238:241], v[82:85]
	v_mfma_f32_16x16x32_f16 v[110:113], v[38:41], v[206:209], v[110:113]
	v_mfma_f32_16x16x32_f16 v[114:117], v[38:41], v[230:233], v[114:117]
	v_mfma_f32_16x16x32_f16 v[118:121], v[38:41], v[234:237], v[118:121]
	v_mfma_f32_16x16x32_f16 v[86:89], v[38:41], v[238:241], v[86:89]
	s_setprio 0
	ds_read_b128 v[34:37], v130 offset:4096
	ds_read_b128 v[38:41], v130 offset:6144
	v_cvt_pk_f16_f32 v1, v12, v13
	v_cvt_pk_f16_f32 v0, v10, v11
	ds_write_b64 v100, v[0:1] offset:53248
	s_add_u32 s80, s22, 0xa0300
	s_addc_u32 s81, s90, 0
	s_add_u32 s100, s22, 0x80300
	s_addc_u32 s101, s90, 0
	global_load_dwordx4 v[14:17], v201, s[100:101] nt
	s_setprio 1
	s_waitcnt lgkmcnt(1)
	v_mfma_f32_16x16x32_f16 v[146:149], v[34:37], v[234:237], v[146:149]
	v_mfma_f32_16x16x32_f16 v[122:125], v[34:37], v[238:241], v[122:125]
	v_mfma_f32_16x16x32_f16 v[134:137], v[38:41], v[238:241], v[134:137]
	v_mfma_f32_16x16x32_f16 v[138:141], v[34:37], v[206:209], v[138:141]
	v_mfma_f32_16x16x32_f16 v[142:145], v[34:37], v[230:233], v[142:145]
	v_mfma_f32_16x16x32_f16 v[150:153], v[38:41], v[206:209], v[150:153]
	v_mfma_f32_16x16x32_f16 v[154:157], v[38:41], v[230:233], v[154:157]
	v_mfma_f32_16x16x32_f16 v[158:161], v[38:41], v[234:237], v[158:161]
	s_setprio 0
	ds_read_b128 v[38:41], v130 offset:8192
	ds_read_b128 v[242:245], v130 offset:10240
	v_cvt_pk_f16_f32 v1, v8, v9
	v_cvt_pk_f16_f32 v0, v6, v7
	ds_write_b64 v100, v[0:1] offset:57344
	s_add_u32 s80, s22, 0xc0300
	s_addc_u32 s81, s90, 0
	s_add_u32 s100, s22, 0xa0300
	s_addc_u32 s101, s90, 0
	global_load_dwordx4 v[10:13], v201, s[100:101] nt
	s_setprio 1
	s_waitcnt lgkmcnt(1)
	v_mfma_f32_16x16x32_f16 v[6:9], v[38:41], v[206:209], v[170:173]
	v_mfma_f32_16x16x32_f16 v[170:173], v[38:41], v[230:233], v[174:177]
	v_mfma_f32_16x16x32_f16 v[174:177], v[38:41], v[234:237], v[178:181]
	v_mfma_f32_16x16x32_f16 v[162:165], v[38:41], v[238:241], v[162:165]
	v_mfma_f32_16x16x32_f16 v[178:181], v[242:245], v[206:209], v[182:185]
	v_mfma_f32_16x16x32_f16 v[182:185], v[242:245], v[230:233], v[186:189]
	v_mfma_f32_16x16x32_f16 v[186:189], v[242:245], v[234:237], v[190:193]
	v_mfma_f32_16x16x32_f16 v[166:169], v[242:245], v[238:241], v[166:169]
	s_setprio 0
	s_nop 0
	ds_read_b128 v[190:193], v130 offset:12288
	ds_read_b128 v[242:245], v130 offset:14336
	v_cvt_pk_f16_f32 v1, v4, v5
	v_cvt_pk_f16_f32 v0, v2, v3
	ds_write_b64 v100, v[0:1] offset:61440
	s_add_u32 s80, s22, 0xe0300
	s_addc_u32 s81, s90, 0
	s_add_u32 s100, s22, 0xc0300
	s_addc_u32 s101, s90, 0
	global_load_dwordx4 v[34:37], v201, s[100:101] nt
	s_add_u32 s100, s22, 0xe0300
	s_addc_u32 s101, s90, 0
	global_load_dwordx4 v[38:41], v201, s[100:101] nt
	s_setprio 1
	s_waitcnt lgkmcnt(1)
	v_mfma_f32_16x16x32_f16 v[78:81], v[242:245], v[238:241], v[78:81]
	v_mfma_f32_16x16x32_f16 v[210:213], v[190:193], v[206:209], v[210:213]
	v_mfma_f32_16x16x32_f16 v[214:217], v[190:193], v[230:233], v[214:217]
	v_mfma_f32_16x16x32_f16 v[218:221], v[190:193], v[234:237], v[218:221]
	v_mfma_f32_16x16x32_f16 v[190:193], v[190:193], v[238:241], v[202:205]
	v_mfma_f32_16x16x32_f16 v[202:205], v[242:245], v[206:209], v[222:225]
	v_mfma_f32_16x16x32_f16 v[206:209], v[242:245], v[230:233], v[226:229]
	v_mfma_f32_16x16x32_f16 v[222:225], v[242:245], v[234:237], v[74:77]
	s_setprio 0
	s_waitcnt vmcnt(6)
	s_waitcnt lgkmcnt(0)
	s_barrier
	ds_read_b128 v[226:229], v131 offset:32768
	ds_read_b128 v[230:233], v131 offset:34816
	ds_read_b128 v[234:237], v131 offset:36864
	ds_read_b128 v[238:241], v131 offset:38912
	ds_read_b128 v[74:77], v129 offset:32768
	ds_read_b128 v[242:245], v129 offset:34816
	s_add_u32 s80, s22, 0x400
	s_addc_u32 s81, s90, 0
	v_lshl_add_u64 v[198:199], s[28:29], 0, v[196:197]
	v_readfirstlane_b32 s70, v94
	s_mov_b32 m0, s70
	v_cvt_pk_f16_f32 v1, v72, v73
	global_load_lds_dwordx4 v[198:199], off
	v_cvt_pk_f16_f32 v0, v70, v71
	ds_write_b64 v100, v[0:1]
	s_setprio 1
	s_waitcnt lgkmcnt(1)
	v_mfma_f32_16x16x32_f16 v[70:73], v[74:77], v[226:229], v[90:93]
	v_mfma_f32_16x16x32_f16 v[90:93], v[74:77], v[230:233], v[102:105]
	v_mfma_f32_16x16x32_f16 v[104:107], v[74:77], v[234:237], v[106:109]
	v_mfma_f32_16x16x32_f16 v[82:85], v[74:77], v[238:241], v[82:85]
	v_mfma_f32_16x16x32_f16 v[108:111], v[242:245], v[226:229], v[110:113]
	v_mfma_f32_16x16x32_f16 v[112:115], v[242:245], v[230:233], v[114:117]
	v_mfma_f32_16x16x32_f16 v[116:119], v[242:245], v[234:237], v[118:121]
	v_mfma_f32_16x16x32_f16 v[86:89], v[242:245], v[238:241], v[86:89]
	s_setprio 0
	ds_read_b128 v[74:77], v129 offset:36864
	ds_read_b128 v[242:245], v129 offset:38912
	v_add_u32_e32 v99, 0x2000, v94
	v_lshl_add_u64 v[4:5], v[198:199], 0, s[58:59]
	v_readfirstlane_b32 s73, v99
	s_mov_b32 m0, s73
	s_nop 0
	global_load_lds_dwordx4 v[4:5], off
	v_cvt_pk_f16_f32 v5, v44, v45
	v_cvt_pk_f16_f32 v4, v42, v43
	ds_write_b64 v100, v[4:5] offset:4096
	s_add_u32 s80, s22, 0x20400
	s_addc_u32 s81, s90, 0
	s_add_u32 s100, s22, 0x400
	s_addc_u32 s101, s90, 0
	global_load_dwordx4 v[0:3], v201, s[100:101] nt
	s_setprio 1
	s_waitcnt lgkmcnt(1)
	v_mfma_f32_16x16x32_f16 v[146:149], v[74:77], v[234:237], v[146:149]
	v_mfma_f32_16x16x32_f16 v[120:123], v[74:77], v[238:241], v[122:125]
	v_mfma_f32_16x16x32_f16 v[124:127], v[242:245], v[226:229], v[150:153]
	v_mfma_f32_16x16x32_f16 v[134:137], v[242:245], v[238:241], v[134:137]
	v_mfma_f32_16x16x32_f16 v[138:141], v[74:77], v[226:229], v[138:141]
	v_mfma_f32_16x16x32_f16 v[142:145], v[74:77], v[230:233], v[142:145]
	v_mfma_f32_16x16x32_f16 v[150:153], v[242:245], v[230:233], v[154:157]
	v_mfma_f32_16x16x32_f16 v[154:157], v[242:245], v[234:237], v[158:161]
	s_setprio 0
	ds_read_b128 v[74:77], v129 offset:40960
	s_nop 0
	ds_read_b128 v[158:161], v129 offset:43008
	v_add_u32_e32 v101, 0x4000, v94
	v_lshl_add_u64 v[4:5], v[198:199], 0, s[60:61]
	v_readfirstlane_b32 s91, v101
	s_mov_b32 m0, s91
	s_nop 0
	global_load_lds_dwordx4 v[4:5], off
	v_cvt_pk_f16_f32 v5, v48, v49
	v_cvt_pk_f16_f32 v4, v46, v47
	ds_write_b64 v100, v[4:5] offset:8192
	s_add_u32 s80, s22, 0x40400
	s_addc_u32 s81, s90, 0
	s_add_u32 s100, s22, 0x20400
	s_addc_u32 s101, s90, 0
	global_load_dwordx4 v[42:45], v201, s[100:101] nt
	s_setprio 1
	s_waitcnt lgkmcnt(1)
	v_mfma_f32_16x16x32_f16 v[4:7], v[74:77], v[226:229], v[6:9]
	v_mfma_f32_16x16x32_f16 v[170:173], v[74:77], v[230:233], v[170:173]
	v_mfma_f32_16x16x32_f16 v[174:177], v[74:77], v[234:237], v[174:177]
	v_mfma_f32_16x16x32_f16 v[162:165], v[74:77], v[238:241], v[162:165]
	v_mfma_f32_16x16x32_f16 v[178:181], v[158:161], v[226:229], v[178:181]
	v_mfma_f32_16x16x32_f16 v[182:185], v[158:161], v[230:233], v[182:185]
	v_mfma_f32_16x16x32_f16 v[186:189], v[158:161], v[234:237], v[186:189]
	v_mfma_f32_16x16x32_f16 v[158:161], v[158:161], v[238:241], v[166:169]
	s_setprio 0
	s_nop 1
	ds_read_b128 v[166:169], v129 offset:45056
	ds_read_b128 v[242:245], v129 offset:47104
	v_add_u32_e32 v102, 0x6000, v94
	v_lshl_add_u64 v[8:9], v[198:199], 0, s[62:63]
	v_readfirstlane_b32 s92, v102
	s_mov_b32 m0, s92
	s_nop 0
	global_load_lds_dwordx4 v[8:9], off
	v_cvt_pk_f16_f32 v9, v68, v69
	v_cvt_pk_f16_f32 v8, v66, v67
	ds_write_b64 v100, v[8:9] offset:12288
	s_add_u32 s80, s22, 0x60400
	s_addc_u32 s81, s90, 0
	s_add_u32 s100, s22, 0x40400
	s_addc_u32 s101, s90, 0
	global_load_dwordx4 v[46:49], v201, s[100:101] nt
	s_setprio 1
	s_waitcnt lgkmcnt(1)
	v_mfma_f32_16x16x32_f16 v[66:69], v[166:169], v[226:229], v[210:213]
	v_mfma_f32_16x16x32_f16 v[210:213], v[166:169], v[230:233], v[214:217]
	v_mfma_f32_16x16x32_f16 v[214:217], v[166:169], v[234:237], v[218:221]
	v_mfma_f32_16x16x32_f16 v[166:169], v[166:169], v[238:241], v[190:193]
	v_mfma_f32_16x16x32_f16 v[190:193], v[242:245], v[226:229], v[202:205]
	v_mfma_f32_16x16x32_f16 v[202:205], v[242:245], v[230:233], v[206:209]
	v_mfma_f32_16x16x32_f16 v[206:209], v[242:245], v[234:237], v[222:225]
	v_mfma_f32_16x16x32_f16 v[218:221], v[242:245], v[238:241], v[78:81]
	s_setprio 0
	s_nop 0
	ds_read_b128 v[222:225], v128 offset:32768
	ds_read_b128 v[226:229], v128 offset:34816
	ds_read_b128 v[230:233], v128 offset:36864
	ds_read_b128 v[234:237], v128 offset:38912
	ds_read_b128 v[238:241], v130 offset:32768
	ds_read_b128 v[242:245], v130 offset:34816
	v_cvt_pk_f16_f32 v9, v64, v65
	v_cvt_pk_f16_f32 v8, v62, v63
	ds_write_b64 v100, v[8:9] offset:16384
	s_add_u32 s80, s22, 0x80400
	s_addc_u32 s81, s90, 0
	s_add_u32 s100, s22, 0x60400
	s_addc_u32 s101, s90, 0
	global_load_dwordx4 v[74:77], v201, s[100:101] nt
	s_setprio 1
	s_waitcnt lgkmcnt(1)
	v_mfma_f32_16x16x32_f16 v[62:65], v[238:241], v[222:225], v[70:73]
	v_mfma_f32_16x16x32_f16 v[70:73], v[238:241], v[226:229], v[90:93]
	v_mfma_f32_16x16x32_f16 v[104:107], v[238:241], v[230:233], v[104:107]
	v_mfma_f32_16x16x32_f16 v[108:111], v[242:245], v[222:225], v[108:111]
	v_mfma_f32_16x16x32_f16 v[112:115], v[242:245], v[226:229], v[112:115]
	v_mfma_f32_16x16x32_f16 v[116:119], v[242:245], v[230:233], v[116:119]
	v_mfma_f32_16x16x32_f16 v[238:241], v[238:241], v[234:237], v[82:85]
	v_mfma_f32_16x16x32_f16 v[242:245], v[242:245], v[234:237], v[86:89]
	s_setprio 0
	s_nop 1
	ds_read_b128 v[86:89], v130 offset:36864
	ds_read_b128 v[90:93], v130 offset:38912
	v_cvt_pk_f16_f32 v9, v60, v61
	v_cvt_pk_f16_f32 v8, v58, v59
	ds_write_b64 v100, v[8:9] offset:20480
	s_add_u32 s80, s22, 0xa0400
	s_addc_u32 s81, s90, 0
	s_add_u32 s100, s22, 0x80400
	s_addc_u32 s101, s90, 0
	global_load_dwordx4 v[78:81], v201, s[100:101] nt
	s_setprio 1
	s_waitcnt lgkmcnt(1)
	v_mfma_f32_16x16x32_f16 v[58:61], v[86:89], v[222:225], v[138:141]
	v_mfma_f32_16x16x32_f16 v[138:141], v[86:89], v[226:229], v[142:145]
	v_mfma_f32_16x16x32_f16 v[142:145], v[86:89], v[230:233], v[146:149]
	v_mfma_f32_16x16x32_f16 v[120:123], v[86:89], v[234:237], v[120:123]
	v_mfma_f32_16x16x32_f16 v[124:127], v[90:93], v[222:225], v[124:127]
	v_mfma_f32_16x16x32_f16 v[146:149], v[90:93], v[226:229], v[150:153]
	v_mfma_f32_16x16x32_f16 v[134:137], v[90:93], v[234:237], v[134:137]
	v_mfma_f32_16x16x32_f16 v[150:153], v[90:93], v[230:233], v[154:157]
	s_setprio 0
	ds_read_b128 v[90:93], v130 offset:40960
	s_nop 0
	ds_read_b128 v[154:157], v130 offset:43008
	v_cvt_pk_f16_f32 v9, v56, v57
	v_cvt_pk_f16_f32 v8, v54, v55
	ds_write_b64 v100, v[8:9] offset:24576
	s_add_u32 s80, s22, 0xc0400
	s_addc_u32 s81, s90, 0
	s_add_u32 s100, s22, 0xa0400
	s_addc_u32 s101, s90, 0
	global_load_dwordx4 v[82:85], v201, s[100:101] nt
	s_setprio 1
	s_waitcnt lgkmcnt(1)
	v_mfma_f32_16x16x32_f16 v[246:249], v[90:93], v[222:225], v[4:7]
	v_mfma_f32_16x16x32_f16 v[170:173], v[90:93], v[226:229], v[170:173]
	v_mfma_f32_16x16x32_f16 v[174:177], v[90:93], v[230:233], v[174:177]
	v_mfma_f32_16x16x32_f16 v[162:165], v[90:93], v[234:237], v[162:165]
	v_mfma_f32_16x16x32_f16 v[178:181], v[154:157], v[222:225], v[178:181]
	v_mfma_f32_16x16x32_f16 v[182:185], v[154:157], v[226:229], v[182:185]
	v_mfma_f32_16x16x32_f16 v[186:189], v[154:157], v[230:233], v[186:189]
	v_mfma_f32_16x16x32_f16 v[154:157], v[154:157], v[234:237], v[158:161]
	s_setprio 0
	ds_read_b128 v[4:7], v130 offset:45056
	ds_read_b128 v[54:57], v130 offset:47104
	v_cvt_pk_f16_f32 v9, v52, v53
	v_cvt_pk_f16_f32 v8, v50, v51
	ds_write_b64 v100, v[8:9] offset:28672
	s_add_u32 s80, s22, 0xe0400
	s_addc_u32 s81, s90, 0
	s_add_u32 s100, s22, 0xc0400
	s_addc_u32 s101, s90, 0
	global_load_dwordx4 v[86:89], v201, s[100:101] nt
	s_add_u32 s100, s22, 0xe0400
	s_addc_u32 s101, s90, 0
	global_load_dwordx4 v[90:93], v201, s[100:101] nt
	s_setprio 1
	s_waitcnt lgkmcnt(1)
	v_mfma_f32_16x16x32_f16 v[66:69], v[4:7], v[222:225], v[66:69]
	v_mfma_f32_16x16x32_f16 v[158:161], v[4:7], v[226:229], v[210:213]
	v_mfma_f32_16x16x32_f16 v[210:213], v[4:7], v[230:233], v[214:217]
	v_mfma_f32_16x16x32_f16 v[166:169], v[4:7], v[234:237], v[166:169]
	v_mfma_f32_16x16x32_f16 v[190:193], v[54:57], v[222:225], v[190:193]
	v_mfma_f32_16x16x32_f16 v[202:205], v[54:57], v[226:229], v[202:205]
	v_mfma_f32_16x16x32_f16 v[206:209], v[54:57], v[230:233], v[206:209]
	v_mfma_f32_16x16x32_f16 v[214:217], v[54:57], v[234:237], v[218:221]
	s_setprio 0
	s_waitcnt vmcnt(6)
	s_waitcnt lgkmcnt(0)
	s_barrier
	s_nop 0
	ds_read_b128 v[218:221], v131
	ds_read_b128 v[222:225], v131 offset:2048
	ds_read_b128 v[226:229], v131 offset:4096
	ds_read_b128 v[230:233], v131 offset:6144
	ds_read_b128 v[50:53], v129
	ds_read_b128 v[54:57], v129 offset:2048
	s_add_u32 s80, s22, 0x500
	v_lshl_add_u64 v[8:9], s[30:31], 0, v[196:197]
	s_addc_u32 s81, s90, 0
	s_mov_b32 m0, s0
	v_cvt_pk_f16_f32 v5, v32, v33
	global_load_lds_dwordx4 v[8:9], off
	v_cvt_pk_f16_f32 v4, v30, v31
	ds_write_b64 v100, v[4:5] offset:32768
	s_setprio 1
	s_waitcnt lgkmcnt(1)
	v_mfma_f32_16x16x32_f16 v[30:33], v[50:53], v[218:221], v[62:65]
	v_mfma_f32_16x16x32_f16 v[70:73], v[50:53], v[222:225], v[70:73]
	v_mfma_f32_16x16x32_f16 v[104:107], v[50:53], v[226:229], v[104:107]
	v_mfma_f32_16x16x32_f16 v[108:111], v[54:57], v[218:221], v[108:111]
	v_mfma_f32_16x16x32_f16 v[112:115], v[54:57], v[222:225], v[112:115]
	v_mfma_f32_16x16x32_f16 v[116:119], v[54:57], v[226:229], v[116:119]
	v_mfma_f32_16x16x32_f16 v[234:237], v[50:53], v[230:233], v[238:241]
	v_mfma_f32_16x16x32_f16 v[238:241], v[54:57], v[230:233], v[242:245]
	s_setprio 0
	ds_read_b128 v[54:57], v129 offset:4096
	ds_read_b128 v[62:65], v129 offset:6144
	s_mov_b32 m0, s1
	v_lshl_add_u64 v[50:51], v[8:9], 0, s[58:59]
	global_load_lds_dwordx4 v[50:51], off
	v_cvt_pk_f16_f32 v29, v28, v29
	v_cvt_pk_f16_f32 v28, v26, v27
	ds_write_b64 v100, v[28:29] offset:36864
	s_add_u32 s0, s22, 0x20500
	s_addc_u32 s1, s90, 0
	s_add_u32 s100, s22, 0x500
	s_addc_u32 s101, s90, 0
	global_load_dwordx4 v[4:7], v201, s[100:101] nt
	s_setprio 1
	s_waitcnt lgkmcnt(1)
	v_mfma_f32_16x16x32_f16 v[26:29], v[54:57], v[218:221], v[58:61]
	v_mfma_f32_16x16x32_f16 v[120:123], v[54:57], v[230:233], v[120:123]
	v_mfma_f32_16x16x32_f16 v[124:127], v[62:65], v[218:221], v[124:127]
	v_mfma_f32_16x16x32_f16 v[146:149], v[62:65], v[222:225], v[146:149]
	v_mfma_f32_16x16x32_f16 v[134:137], v[62:65], v[230:233], v[134:137]
	v_mfma_f32_16x16x32_f16 v[138:141], v[54:57], v[222:225], v[138:141]
	v_mfma_f32_16x16x32_f16 v[142:145], v[54:57], v[226:229], v[142:145]
	v_mfma_f32_16x16x32_f16 v[150:153], v[62:65], v[226:229], v[150:153]
	s_setprio 0
	ds_read_b128 v[58:61], v129 offset:8192
	ds_read_b128 v[62:65], v129 offset:10240
	s_mov_b32 m0, s71
	v_lshl_add_u64 v[54:55], v[8:9], 0, s[60:61]
	global_load_lds_dwordx4 v[54:55], off
	v_cvt_pk_f16_f32 v25, v24, v25
	v_cvt_pk_f16_f32 v24, v22, v23
	ds_write_b64 v100, v[24:25] offset:40960
	s_add_u32 s0, s22, 0x40500
	s_addc_u32 s1, s90, 0
	s_add_u32 s100, s22, 0x20500
	s_addc_u32 s101, s90, 0
	global_load_dwordx4 v[50:53], v201, s[100:101] nt
	s_setprio 1
	s_waitcnt lgkmcnt(1)
	v_mfma_f32_16x16x32_f16 v[22:25], v[58:61], v[218:221], v[246:249]
	v_mfma_f32_16x16x32_f16 v[170:173], v[58:61], v[222:225], v[170:173]
	v_mfma_f32_16x16x32_f16 v[174:177], v[58:61], v[226:229], v[174:177]
	v_mfma_f32_16x16x32_f16 v[162:165], v[58:61], v[230:233], v[162:165]
	v_mfma_f32_16x16x32_f16 v[178:181], v[62:65], v[218:221], v[178:181]
	v_mfma_f32_16x16x32_f16 v[182:185], v[62:65], v[222:225], v[182:185]
	v_mfma_f32_16x16x32_f16 v[186:189], v[62:65], v[226:229], v[186:189]
	v_mfma_f32_16x16x32_f16 v[154:157], v[62:65], v[230:233], v[154:157]
	s_setprio 0
	ds_read_b128 v[62:65], v129 offset:12288
	ds_read_b128 v[242:245], v129 offset:14336
	s_mov_b32 m0, s72
	v_lshl_add_u64 v[8:9], v[8:9], 0, s[62:63]
	global_load_lds_dwordx4 v[8:9], off
	v_cvt_pk_f16_f32 v9, v20, v21
	v_cvt_pk_f16_f32 v8, v18, v19
	ds_write_b64 v100, v[8:9] offset:45056
	s_add_u32 s0, s22, 0x60500
	s_addc_u32 s1, s90, 0
	s_add_u32 s100, s22, 0x40500
	s_addc_u32 s101, s90, 0
	global_load_dwordx4 v[54:57], v201, s[100:101] nt
	s_setprio 1
	s_waitcnt lgkmcnt(1)
	v_mfma_f32_16x16x32_f16 v[18:21], v[62:65], v[218:221], v[66:69]
	v_mfma_f32_16x16x32_f16 v[158:161], v[62:65], v[222:225], v[158:161]
	v_mfma_f32_16x16x32_f16 v[210:213], v[62:65], v[226:229], v[210:213]
	v_mfma_f32_16x16x32_f16 v[166:169], v[62:65], v[230:233], v[166:169]
	v_mfma_f32_16x16x32_f16 v[190:193], v[242:245], v[218:221], v[190:193]
	v_mfma_f32_16x16x32_f16 v[202:205], v[242:245], v[222:225], v[202:205]
	v_mfma_f32_16x16x32_f16 v[206:209], v[242:245], v[226:229], v[206:209]
	v_mfma_f32_16x16x32_f16 v[214:217], v[242:245], v[230:233], v[214:217]
	s_setprio 0
	ds_read_b128 v[218:221], v128
	ds_read_b128 v[222:225], v128 offset:2048
	ds_read_b128 v[226:229], v128 offset:4096
	ds_read_b128 v[230:233], v128 offset:6144
	ds_read_b128 v[66:69], v130
	ds_read_b128 v[242:245], v130 offset:2048
	v_cvt_pk_f16_f32 v9, v16, v17
	v_cvt_pk_f16_f32 v8, v14, v15
	ds_write_b64 v100, v[8:9] offset:49152
	s_add_u32 s0, s22, 0x80500
	s_addc_u32 s1, s90, 0
	s_add_u32 s100, s22, 0x60500
	s_addc_u32 s101, s90, 0
	global_load_dwordx4 v[58:61], v201, s[100:101] nt
	s_setprio 1
	s_waitcnt lgkmcnt(1)
	v_mfma_f32_16x16x32_f16 v[14:17], v[66:69], v[218:221], v[30:33]
	v_mfma_f32_16x16x32_f16 v[30:33], v[66:69], v[222:225], v[70:73]
	v_mfma_f32_16x16x32_f16 v[104:107], v[66:69], v[226:229], v[104:107]
	v_mfma_f32_16x16x32_f16 v[108:111], v[242:245], v[218:221], v[108:111]
	v_mfma_f32_16x16x32_f16 v[112:115], v[242:245], v[222:225], v[112:115]
	v_mfma_f32_16x16x32_f16 v[116:119], v[242:245], v[226:229], v[116:119]
	v_mfma_f32_16x16x32_f16 v[234:237], v[66:69], v[230:233], v[234:237]
	v_mfma_f32_16x16x32_f16 v[238:241], v[242:245], v[230:233], v[238:241]
	s_setprio 0
	ds_read_b128 v[70:73], v130 offset:4096
	ds_read_b128 v[242:245], v130 offset:6144
	v_cvt_pk_f16_f32 v9, v12, v13
	v_cvt_pk_f16_f32 v8, v10, v11
	ds_write_b64 v100, v[8:9] offset:53248
	s_add_u32 s0, s22, 0xa0500
	s_addc_u32 s1, s90, 0
	s_add_u32 s100, s22, 0x80500
	s_addc_u32 s101, s90, 0
	global_load_dwordx4 v[62:65], v201, s[100:101] nt
	s_setprio 1
	s_waitcnt lgkmcnt(1)
	v_mfma_f32_16x16x32_f16 v[26:29], v[70:73], v[218:221], v[26:29]
	v_mfma_f32_16x16x32_f16 v[120:123], v[70:73], v[230:233], v[120:123]
	v_mfma_f32_16x16x32_f16 v[124:127], v[242:245], v[218:221], v[124:127]
	v_mfma_f32_16x16x32_f16 v[146:149], v[242:245], v[222:225], v[146:149]
	v_mfma_f32_16x16x32_f16 v[134:137], v[242:245], v[230:233], v[134:137]
	v_mfma_f32_16x16x32_f16 v[138:141], v[70:73], v[222:225], v[138:141]
	v_mfma_f32_16x16x32_f16 v[142:145], v[70:73], v[226:229], v[142:145]
	v_mfma_f32_16x16x32_f16 v[150:153], v[242:245], v[226:229], v[150:153]
	s_setprio 0
	ds_read_b128 v[8:11], v130 offset:8192
	ds_read_b128 v[242:245], v130 offset:10240
	v_cvt_pk_f16_f32 v13, v36, v37
	v_cvt_pk_f16_f32 v12, v34, v35
	ds_write_b64 v100, v[12:13] offset:57344
	s_add_u32 s0, s22, 0xc0500
	s_addc_u32 s1, s90, 0
	s_add_u32 s100, s22, 0xa0500
	s_addc_u32 s101, s90, 0
	global_load_dwordx4 v[66:69], v201, s[100:101] nt
	s_setprio 1
	s_waitcnt lgkmcnt(1)
	v_mfma_f32_16x16x32_f16 v[22:25], v[8:11], v[218:221], v[22:25]
	v_mfma_f32_16x16x32_f16 v[170:173], v[8:11], v[222:225], v[170:173]
	v_mfma_f32_16x16x32_f16 v[174:177], v[8:11], v[226:229], v[174:177]
	v_mfma_f32_16x16x32_f16 v[162:165], v[8:11], v[230:233], v[162:165]
	v_mfma_f32_16x16x32_f16 v[178:181], v[242:245], v[218:221], v[178:181]
	v_mfma_f32_16x16x32_f16 v[182:185], v[242:245], v[222:225], v[182:185]
	v_mfma_f32_16x16x32_f16 v[186:189], v[242:245], v[226:229], v[186:189]
	v_mfma_f32_16x16x32_f16 v[154:157], v[242:245], v[230:233], v[154:157]
	s_setprio 0
	ds_read_b128 v[8:11], v130 offset:12288
	ds_read_b128 v[242:245], v130 offset:14336
	v_cvt_pk_f16_f32 v13, v40, v41
	v_cvt_pk_f16_f32 v12, v38, v39
	ds_write_b64 v100, v[12:13] offset:61440
	s_add_u32 s0, s22, 0xe0500
	s_addc_u32 s1, s90, 0
	s_add_u32 s100, s22, 0xc0500
	s_addc_u32 s101, s90, 0
	global_load_dwordx4 v[70:73], v201, s[100:101] nt
	s_add_u32 s100, s22, 0xe0500
	s_addc_u32 s101, s90, 0
	global_load_dwordx4 v[36:39], v201, s[100:101] nt
	s_setprio 1
	s_waitcnt lgkmcnt(1)
	v_mfma_f32_16x16x32_f16 v[246:249], v[8:11], v[218:221], v[18:21]
	v_mfma_f32_16x16x32_f16 v[158:161], v[8:11], v[222:225], v[158:161]
	v_mfma_f32_16x16x32_f16 v[210:213], v[8:11], v[226:229], v[210:213]
	v_mfma_f32_16x16x32_f16 v[166:169], v[8:11], v[230:233], v[166:169]
	v_mfma_f32_16x16x32_f16 v[190:193], v[242:245], v[218:221], v[190:193]
	v_mfma_f32_16x16x32_f16 v[202:205], v[242:245], v[222:225], v[202:205]
	v_mfma_f32_16x16x32_f16 v[206:209], v[242:245], v[226:229], v[206:209]
	v_mfma_f32_16x16x32_f16 v[214:217], v[242:245], v[230:233], v[214:217]
	s_setprio 0
	s_waitcnt vmcnt(6)
	s_waitcnt lgkmcnt(0)
	s_barrier
	ds_read_b128 v[218:221], v131 offset:32768
	ds_read_b128 v[222:225], v131 offset:34816
	ds_read_b128 v[226:229], v131 offset:36864
	ds_read_b128 v[230:233], v131 offset:38912
	ds_read_b128 v[8:11], v129 offset:32768
	ds_read_b128 v[18:21], v129 offset:34816
	s_add_u32 s0, s22, 0x600
	s_addc_u32 s1, s90, 0
	v_lshl_add_u64 v[34:35], s[34:35], 0, v[196:197]
	s_mov_b32 m0, s70
	v_cvt_pk_f16_f32 v3, v2, v3
	global_load_lds_dwordx4 v[34:35], off
	v_cvt_pk_f16_f32 v2, v0, v1
	ds_write_b64 v100, v[2:3]
	s_setprio 1
	s_waitcnt lgkmcnt(1)
	v_mfma_f32_16x16x32_f16 v[30:33], v[8:11], v[222:225], v[30:33]
	v_mfma_f32_16x16x32_f16 v[104:107], v[8:11], v[226:229], v[104:107]
	v_mfma_f32_16x16x32_f16 v[108:111], v[18:21], v[218:221], v[108:111]
	v_mfma_f32_16x16x32_f16 v[112:115], v[18:21], v[222:225], v[112:115]
	v_mfma_f32_16x16x32_f16 v[116:119], v[18:21], v[226:229], v[116:119]
	v_mfma_f32_16x16x32_f16 v[242:245], v[8:11], v[218:221], v[14:17]
	v_mfma_f32_16x16x32_f16 v[234:237], v[8:11], v[230:233], v[234:237]
	v_mfma_f32_16x16x32_f16 v[238:241], v[18:21], v[230:233], v[238:241]
	s_setprio 0
	ds_read_b128 v[12:15], v129 offset:36864
	ds_read_b128 v[16:19], v129 offset:38912
	s_mov_b32 m0, s73
	v_lshl_add_u64 v[8:9], v[34:35], 0, s[58:59]
	global_load_lds_dwordx4 v[8:9], off
	v_cvt_pk_f16_f32 v9, v44, v45
	v_cvt_pk_f16_f32 v8, v42, v43
	ds_write_b64 v100, v[8:9] offset:4096
	s_add_u32 s0, s22, 0x20600
	s_addc_u32 s1, s90, 0
	s_add_u32 s100, s22, 0x600
	s_addc_u32 s101, s90, 0
	global_load_dwordx4 v[0:3], v201, s[100:101] nt
	s_setprio 1
	s_waitcnt lgkmcnt(1)
	v_mfma_f32_16x16x32_f16 v[40:43], v[12:15], v[218:221], v[26:29]
	v_mfma_f32_16x16x32_f16 v[120:123], v[12:15], v[230:233], v[120:123]
	v_mfma_f32_16x16x32_f16 v[124:127], v[16:19], v[218:221], v[124:127]
	v_mfma_f32_16x16x32_f16 v[146:149], v[16:19], v[222:225], v[146:149]
	v_mfma_f32_16x16x32_f16 v[134:137], v[16:19], v[230:233], v[134:137]
	v_mfma_f32_16x16x32_f16 v[138:141], v[12:15], v[222:225], v[138:141]
	v_mfma_f32_16x16x32_f16 v[142:145], v[12:15], v[226:229], v[142:145]
	v_mfma_f32_16x16x32_f16 v[150:153], v[16:19], v[226:229], v[150:153]
	s_setprio 0
	ds_read_b128 v[16:19], v129 offset:40960
	ds_read_b128 v[26:29], v129 offset:43008
	s_mov_b32 m0, s91
	v_lshl_add_u64 v[12:13], v[34:35], 0, s[60:61]
	global_load_lds_dwordx4 v[12:13], off
	v_cvt_pk_f16_f32 v13, v48, v49
	v_cvt_pk_f16_f32 v12, v46, v47
	ds_write_b64 v100, v[12:13] offset:8192
	s_add_u32 s0, s22, 0x40600
	s_addc_u32 s1, s90, 0
	s_add_u32 s100, s22, 0x20600
	s_addc_u32 s101, s90, 0
	global_load_dwordx4 v[8:11], v201, s[100:101] nt
	s_setprio 1
	s_waitcnt lgkmcnt(1)
	v_mfma_f32_16x16x32_f16 v[44:47], v[16:19], v[218:221], v[22:25]
	v_mfma_f32_16x16x32_f16 v[170:173], v[16:19], v[222:225], v[170:173]
	v_mfma_f32_16x16x32_f16 v[174:177], v[16:19], v[226:229], v[174:177]
	v_mfma_f32_16x16x32_f16 v[162:165], v[16:19], v[230:233], v[162:165]
	v_mfma_f32_16x16x32_f16 v[178:181], v[26:29], v[218:221], v[178:181]
	v_mfma_f32_16x16x32_f16 v[182:185], v[26:29], v[222:225], v[182:185]
	v_mfma_f32_16x16x32_f16 v[186:189], v[26:29], v[226:229], v[186:189]
	v_mfma_f32_16x16x32_f16 v[154:157], v[26:29], v[230:233], v[154:157]
	s_setprio 0
	ds_read_b128 v[20:23], v129 offset:45056
	ds_read_b128 v[24:27], v129 offset:47104
	s_mov_b32 m0, s92
	v_lshl_add_u64 v[16:17], v[34:35], 0, s[62:63]
	global_load_lds_dwordx4 v[16:17], off
	v_cvt_pk_f16_f32 v17, v76, v77
	v_cvt_pk_f16_f32 v16, v74, v75
	ds_write_b64 v100, v[16:17] offset:12288
	s_add_u32 s0, s22, 0x60600
	s_addc_u32 s1, s90, 0
	s_add_u32 s100, s22, 0x40600
	s_addc_u32 s101, s90, 0
	global_load_dwordx4 v[12:15], v201, s[100:101] nt
	s_setprio 1
	s_waitcnt lgkmcnt(1)
	v_mfma_f32_16x16x32_f16 v[74:77], v[20:23], v[218:221], v[246:249]
	v_mfma_f32_16x16x32_f16 v[158:161], v[20:23], v[222:225], v[158:161]
	v_mfma_f32_16x16x32_f16 v[210:213], v[20:23], v[226:229], v[210:213]
	v_mfma_f32_16x16x32_f16 v[166:169], v[20:23], v[230:233], v[166:169]
	v_mfma_f32_16x16x32_f16 v[190:193], v[24:27], v[218:221], v[190:193]
	v_mfma_f32_16x16x32_f16 v[202:205], v[24:27], v[222:225], v[202:205]
	v_mfma_f32_16x16x32_f16 v[206:209], v[24:27], v[226:229], v[206:209]
	v_mfma_f32_16x16x32_f16 v[214:217], v[24:27], v[230:233], v[214:217]
	s_setprio 0
	ds_read_b128 v[218:221], v128 offset:32768
	ds_read_b128 v[222:225], v128 offset:34816
	ds_read_b128 v[226:229], v128 offset:36864
	ds_read_b128 v[230:233], v128 offset:38912
	ds_read_b128 v[24:27], v130 offset:32768
	ds_read_b128 v[246:249], v130 offset:34816
	v_cvt_pk_f16_f32 v21, v80, v81
	v_cvt_pk_f16_f32 v20, v78, v79
	ds_write_b64 v100, v[20:21] offset:16384
	s_add_u32 s0, s22, 0x80600
	s_addc_u32 s1, s90, 0
	s_add_u32 s100, s22, 0x60600
	s_addc_u32 s101, s90, 0
	global_load_dwordx4 v[16:19], v201, s[100:101] nt
	s_setprio 1
	s_waitcnt lgkmcnt(1)
	v_mfma_f32_16x16x32_f16 v[78:81], v[24:27], v[218:221], v[242:245]
	v_mfma_f32_16x16x32_f16 v[104:107], v[24:27], v[226:229], v[104:107]
	v_mfma_f32_16x16x32_f16 v[108:111], v[246:249], v[218:221], v[108:111]
	v_mfma_f32_16x16x32_f16 v[112:115], v[246:249], v[222:225], v[112:115]
	v_mfma_f32_16x16x32_f16 v[116:119], v[246:249], v[226:229], v[116:119]
	v_mfma_f32_16x16x32_f16 v[242:245], v[24:27], v[222:225], v[30:33]
	v_mfma_f32_16x16x32_f16 v[234:237], v[24:27], v[230:233], v[234:237]
	v_mfma_f32_16x16x32_f16 v[238:241], v[246:249], v[230:233], v[238:241]
	s_setprio 0
	ds_read_b128 v[28:31], v130 offset:36864
	ds_read_b128 v[32:35], v130 offset:38912
	v_cvt_pk_f16_f32 v25, v84, v85
	v_cvt_pk_f16_f32 v24, v82, v83
	ds_write_b64 v100, v[24:25] offset:20480
	s_add_u32 s0, s22, 0xa0600
	s_addc_u32 s1, s90, 0
	s_add_u32 s100, s22, 0x80600
	s_addc_u32 s101, s90, 0
	global_load_dwordx4 v[20:23], v201, s[100:101] nt
	s_setprio 1
	s_waitcnt lgkmcnt(1)
	v_mfma_f32_16x16x32_f16 v[82:85], v[28:31], v[218:221], v[40:43]
	v_mfma_f32_16x16x32_f16 v[120:123], v[28:31], v[230:233], v[120:123]
	v_mfma_f32_16x16x32_f16 v[124:127], v[32:35], v[218:221], v[124:127]
	v_mfma_f32_16x16x32_f16 v[146:149], v[32:35], v[222:225], v[146:149]
	v_mfma_f32_16x16x32_f16 v[134:137], v[32:35], v[230:233], v[134:137]
	v_mfma_f32_16x16x32_f16 v[138:141], v[28:31], v[222:225], v[138:141]
	v_mfma_f32_16x16x32_f16 v[142:145], v[28:31], v[226:229], v[142:145]
	v_mfma_f32_16x16x32_f16 v[150:153], v[32:35], v[226:229], v[150:153]
	s_setprio 0
	ds_read_b128 v[32:35], v130 offset:40960
	ds_read_b128 v[40:43], v130 offset:43008
	v_cvt_pk_f16_f32 v29, v88, v89
	v_cvt_pk_f16_f32 v28, v86, v87
	ds_write_b64 v100, v[28:29] offset:24576
	s_add_u32 s0, s22, 0xc0600
	s_addc_u32 s1, s90, 0
	s_add_u32 s100, s22, 0xa0600
	s_addc_u32 s101, s90, 0
	global_load_dwordx4 v[24:27], v201, s[100:101] nt
	s_setprio 1
	s_waitcnt lgkmcnt(1)
	v_mfma_f32_16x16x32_f16 v[86:89], v[32:35], v[218:221], v[44:47]
	v_mfma_f32_16x16x32_f16 v[170:173], v[32:35], v[222:225], v[170:173]
	v_mfma_f32_16x16x32_f16 v[174:177], v[32:35], v[226:229], v[174:177]
	v_mfma_f32_16x16x32_f16 v[162:165], v[32:35], v[230:233], v[162:165]
	v_mfma_f32_16x16x32_f16 v[178:181], v[40:43], v[218:221], v[178:181]
	v_mfma_f32_16x16x32_f16 v[182:185], v[40:43], v[222:225], v[182:185]
	v_mfma_f32_16x16x32_f16 v[186:189], v[40:43], v[226:229], v[186:189]
	v_mfma_f32_16x16x32_f16 v[154:157], v[40:43], v[230:233], v[154:157]
	s_setprio 0
	ds_read_b128 v[40:43], v130 offset:45056
	ds_read_b128 v[44:47], v130 offset:47104
	v_cvt_pk_f16_f32 v33, v92, v93
	v_cvt_pk_f16_f32 v32, v90, v91
	ds_write_b64 v100, v[32:33] offset:28672
	s_add_u32 s0, s22, 0xe0600
	s_addc_u32 s1, s90, 0
	s_add_u32 s100, s22, 0xc0600
	s_addc_u32 s101, s90, 0
	global_load_dwordx4 v[28:31], v201, s[100:101] nt
	s_add_u32 s100, s22, 0xe0600
	s_addc_u32 s101, s90, 0
	global_load_dwordx4 v[32:35], v201, s[100:101] nt
	s_setprio 1
	s_waitcnt lgkmcnt(1)
	v_mfma_f32_16x16x32_f16 v[74:77], v[40:43], v[218:221], v[74:77]
	v_mfma_f32_16x16x32_f16 v[90:93], v[40:43], v[222:225], v[158:161]
	v_mfma_f32_16x16x32_f16 v[158:161], v[40:43], v[226:229], v[210:213]
	v_mfma_f32_16x16x32_f16 v[166:169], v[40:43], v[230:233], v[166:169]
	v_mfma_f32_16x16x32_f16 v[190:193], v[44:47], v[218:221], v[190:193]
	v_mfma_f32_16x16x32_f16 v[202:205], v[44:47], v[222:225], v[202:205]
	v_mfma_f32_16x16x32_f16 v[206:209], v[44:47], v[226:229], v[206:209]
	v_mfma_f32_16x16x32_f16 v[210:213], v[44:47], v[230:233], v[214:217]
	s_setprio 0
	s_waitcnt vmcnt(6)
	s_waitcnt lgkmcnt(0)
	s_barrier
	s_nop 0
	ds_read_b128 v[214:217], v131
	ds_read_b128 v[218:221], v131 offset:2048
	ds_read_b128 v[222:225], v131 offset:4096
	ds_read_b128 v[226:229], v131 offset:6144
	ds_read_b128 v[40:43], v129
	ds_read_b128 v[44:47], v129 offset:2048
	s_add_u32 s70, s22, 0x700
	s_addc_u32 s71, s90, 0
	v_lshl_add_u64 v[198:199], s[36:37], 0, v[196:197]
	v_readfirstlane_b32 s0, v95
	s_mov_b32 m0, s0
	v_cvt_pk_f16_f32 v7, v6, v7
	global_load_lds_dwordx4 v[198:199], off
	v_cvt_pk_f16_f32 v6, v4, v5
	ds_write_b64 v100, v[6:7] offset:32768
	s_setprio 1
	s_waitcnt lgkmcnt(1)
	v_mfma_f32_16x16x32_f16 v[78:81], v[40:43], v[214:217], v[78:81]
	v_mfma_f32_16x16x32_f16 v[104:107], v[40:43], v[222:225], v[104:107]
	v_mfma_f32_16x16x32_f16 v[108:111], v[44:47], v[214:217], v[108:111]
	v_mfma_f32_16x16x32_f16 v[112:115], v[44:47], v[218:221], v[112:115]
	v_mfma_f32_16x16x32_f16 v[116:119], v[44:47], v[222:225], v[116:119]
	v_mfma_f32_16x16x32_f16 v[230:233], v[40:43], v[218:221], v[242:245]
	v_mfma_f32_16x16x32_f16 v[234:237], v[40:43], v[226:229], v[234:237]
	v_mfma_f32_16x16x32_f16 v[238:241], v[44:47], v[226:229], v[238:241]
	s_setprio 0
	ds_read_b128 v[44:47], v129 offset:4096
	ds_read_b128 v[242:245], v129 offset:6144
	v_readfirstlane_b32 s72, v96
	v_lshl_add_u64 v[40:41], v[198:199], 0, s[58:59]
	s_mov_b32 m0, s72
	s_nop 0
	global_load_lds_dwordx4 v[40:41], off
	v_cvt_pk_f16_f32 v41, v52, v53
	v_cvt_pk_f16_f32 v40, v50, v51
	ds_write_b64 v100, v[40:41] offset:36864
	s_add_u32 s70, s22, 0x20700
	s_addc_u32 s71, s90, 0
	s_add_u32 s100, s22, 0x700
	s_addc_u32 s101, s90, 0
	global_load_dwordx4 v[4:7], v201, s[100:101] nt
	s_setprio 1
	s_waitcnt lgkmcnt(1)
	v_mfma_f32_16x16x32_f16 v[82:85], v[44:47], v[214:217], v[82:85]
	v_mfma_f32_16x16x32_f16 v[120:123], v[44:47], v[226:229], v[120:123]
	v_mfma_f32_16x16x32_f16 v[124:127], v[242:245], v[214:217], v[124:127]
	v_mfma_f32_16x16x32_f16 v[146:149], v[242:245], v[218:221], v[146:149]
	v_mfma_f32_16x16x32_f16 v[134:137], v[242:245], v[226:229], v[134:137]
	v_mfma_f32_16x16x32_f16 v[138:141], v[44:47], v[218:221], v[138:141]
	v_mfma_f32_16x16x32_f16 v[142:145], v[44:47], v[222:225], v[142:145]
	v_mfma_f32_16x16x32_f16 v[150:153], v[242:245], v[222:225], v[150:153]
	s_setprio 0
	ds_read_b128 v[48:51], v129 offset:8192
	ds_read_b128 v[242:245], v129 offset:10240
	v_readfirstlane_b32 s71, v97
	v_lshl_add_u64 v[44:45], v[198:199], 0, s[60:61]
	s_mov_b32 m0, s71
	s_nop 0
	global_load_lds_dwordx4 v[44:45], off
	v_cvt_pk_f16_f32 v45, v56, v57
	v_cvt_pk_f16_f32 v44, v54, v55
	ds_write_b64 v100, v[44:45] offset:40960
	s_add_u32 s80, s22, 0x40700
	s_addc_u32 s81, s90, 0
	s_add_u32 s100, s22, 0x20700
	s_addc_u32 s101, s90, 0
	global_load_dwordx4 v[40:43], v201, s[100:101] nt
	s_setprio 1
	s_waitcnt lgkmcnt(1)
	v_mfma_f32_16x16x32_f16 v[86:89], v[48:51], v[214:217], v[86:89]
	v_mfma_f32_16x16x32_f16 v[170:173], v[48:51], v[218:221], v[170:173]
	v_mfma_f32_16x16x32_f16 v[174:177], v[48:51], v[222:225], v[174:177]
	v_mfma_f32_16x16x32_f16 v[162:165], v[48:51], v[226:229], v[162:165]
	v_mfma_f32_16x16x32_f16 v[178:181], v[242:245], v[214:217], v[178:181]
	v_mfma_f32_16x16x32_f16 v[182:185], v[242:245], v[218:221], v[182:185]
	v_mfma_f32_16x16x32_f16 v[186:189], v[242:245], v[222:225], v[186:189]
	v_mfma_f32_16x16x32_f16 v[154:157], v[242:245], v[226:229], v[154:157]
	s_setprio 0
	ds_read_b128 v[52:55], v129 offset:12288
	ds_read_b128 v[242:245], v129 offset:14336
	v_readfirstlane_b32 s70, v98
	v_lshl_add_u64 v[48:49], v[198:199], 0, s[62:63]
	s_mov_b32 m0, s70
	s_nop 0
	global_load_lds_dwordx4 v[48:49], off
	v_cvt_pk_f16_f32 v49, v60, v61
	v_cvt_pk_f16_f32 v48, v58, v59
	ds_write_b64 v100, v[48:49] offset:45056
	s_add_u32 s80, s22, 0x60700
	s_addc_u32 s81, s90, 0
	s_add_u32 s100, s22, 0x40700
	s_addc_u32 s101, s90, 0
	global_load_dwordx4 v[44:47], v201, s[100:101] nt
	s_setprio 1
	s_waitcnt lgkmcnt(1)
	v_mfma_f32_16x16x32_f16 v[74:77], v[52:55], v[214:217], v[74:77]
	v_mfma_f32_16x16x32_f16 v[90:93], v[52:55], v[218:221], v[90:93]
	v_mfma_f32_16x16x32_f16 v[158:161], v[52:55], v[222:225], v[158:161]
	v_mfma_f32_16x16x32_f16 v[166:169], v[52:55], v[226:229], v[166:169]
	v_mfma_f32_16x16x32_f16 v[190:193], v[242:245], v[214:217], v[190:193]
	v_mfma_f32_16x16x32_f16 v[202:205], v[242:245], v[218:221], v[202:205]
	v_mfma_f32_16x16x32_f16 v[206:209], v[242:245], v[222:225], v[206:209]
	v_mfma_f32_16x16x32_f16 v[210:213], v[242:245], v[226:229], v[210:213]
	s_setprio 0
	ds_read_b128 v[214:217], v128
	ds_read_b128 v[218:221], v128 offset:2048
	ds_read_b128 v[222:225], v128 offset:4096
	ds_read_b128 v[226:229], v128 offset:6144
	ds_read_b128 v[56:59], v130
	ds_read_b128 v[242:245], v130 offset:2048
	v_cvt_pk_f16_f32 v53, v64, v65
	v_cvt_pk_f16_f32 v52, v62, v63
	ds_write_b64 v100, v[52:53] offset:49152
	s_add_u32 s80, s22, 0x80700
	s_addc_u32 s81, s90, 0
	s_add_u32 s100, s22, 0x60700
	s_addc_u32 s101, s90, 0
	global_load_dwordx4 v[48:51], v201, s[100:101] nt
	s_setprio 1
	s_waitcnt lgkmcnt(1)
	v_mfma_f32_16x16x32_f16 v[78:81], v[56:59], v[214:217], v[78:81]
	v_mfma_f32_16x16x32_f16 v[104:107], v[56:59], v[222:225], v[104:107]
	v_mfma_f32_16x16x32_f16 v[108:111], v[242:245], v[214:217], v[108:111]
	v_mfma_f32_16x16x32_f16 v[112:115], v[242:245], v[218:221], v[112:115]
	v_mfma_f32_16x16x32_f16 v[116:119], v[242:245], v[222:225], v[116:119]
	v_mfma_f32_16x16x32_f16 v[230:233], v[56:59], v[218:221], v[230:233]
	v_mfma_f32_16x16x32_f16 v[234:237], v[56:59], v[226:229], v[234:237]
	v_mfma_f32_16x16x32_f16 v[238:241], v[242:245], v[226:229], v[238:241]
	s_setprio 0
	ds_read_b128 v[60:63], v130 offset:4096
	ds_read_b128 v[242:245], v130 offset:6144
	v_cvt_pk_f16_f32 v57, v68, v69
	v_cvt_pk_f16_f32 v56, v66, v67
	ds_write_b64 v100, v[56:57] offset:53248
	s_add_u32 s80, s22, 0xa0700
	s_addc_u32 s81, s90, 0
	s_add_u32 s100, s22, 0x80700
	s_addc_u32 s101, s90, 0
	global_load_dwordx4 v[52:55], v201, s[100:101] nt
	s_setprio 1
	s_waitcnt lgkmcnt(1)
	v_mfma_f32_16x16x32_f16 v[82:85], v[60:63], v[214:217], v[82:85]
	v_mfma_f32_16x16x32_f16 v[120:123], v[60:63], v[226:229], v[120:123]
	v_mfma_f32_16x16x32_f16 v[124:127], v[242:245], v[214:217], v[124:127]
	v_mfma_f32_16x16x32_f16 v[146:149], v[242:245], v[218:221], v[146:149]
	v_mfma_f32_16x16x32_f16 v[134:137], v[242:245], v[226:229], v[134:137]
	v_mfma_f32_16x16x32_f16 v[138:141], v[60:63], v[218:221], v[138:141]
	v_mfma_f32_16x16x32_f16 v[142:145], v[60:63], v[222:225], v[142:145]
	v_mfma_f32_16x16x32_f16 v[150:153], v[242:245], v[222:225], v[150:153]
	s_setprio 0
	ds_read_b128 v[64:67], v130 offset:8192
	ds_read_b128 v[242:245], v130 offset:10240
	v_cvt_pk_f16_f32 v61, v72, v73
	v_cvt_pk_f16_f32 v60, v70, v71
	ds_write_b64 v100, v[60:61] offset:57344
	s_add_u32 s80, s22, 0xc0700
	s_addc_u32 s81, s90, 0
	s_add_u32 s100, s22, 0xa0700
	s_addc_u32 s101, s90, 0
	global_load_dwordx4 v[56:59], v201, s[100:101] nt
	s_setprio 1
	s_waitcnt lgkmcnt(1)
	v_mfma_f32_16x16x32_f16 v[86:89], v[64:67], v[214:217], v[86:89]
	v_mfma_f32_16x16x32_f16 v[170:173], v[64:67], v[218:221], v[170:173]
	v_mfma_f32_16x16x32_f16 v[174:177], v[64:67], v[222:225], v[174:177]
	v_mfma_f32_16x16x32_f16 v[162:165], v[64:67], v[226:229], v[162:165]
	v_mfma_f32_16x16x32_f16 v[178:181], v[242:245], v[214:217], v[178:181]
	v_mfma_f32_16x16x32_f16 v[182:185], v[242:245], v[218:221], v[182:185]
	v_mfma_f32_16x16x32_f16 v[186:189], v[242:245], v[222:225], v[186:189]
	v_mfma_f32_16x16x32_f16 v[154:157], v[242:245], v[226:229], v[154:157]
	s_setprio 0
	ds_read_b128 v[64:67], v130 offset:12288
	ds_read_b128 v[68:71], v130 offset:14336
	v_cvt_pk_f16_f32 v39, v38, v39
	v_cvt_pk_f16_f32 v38, v36, v37
	ds_write_b64 v100, v[38:39] offset:61440
	s_add_u32 s80, s22, 0xe0700
	s_addc_u32 s81, s90, 0
	s_add_u32 s100, s22, 0xc0700
	s_addc_u32 s101, s90, 0
	global_load_dwordx4 v[60:63], v201, s[100:101] nt
	s_add_u32 s100, s22, 0xe0700
	s_addc_u32 s101, s90, 0
	global_load_dwordx4 v[36:39], v201, s[100:101] nt
	s_setprio 1
	s_waitcnt lgkmcnt(1)
	v_mfma_f32_16x16x32_f16 v[90:93], v[64:67], v[218:221], v[90:93]
	v_mfma_f32_16x16x32_f16 v[242:245], v[64:67], v[214:217], v[74:77]
	v_mfma_f32_16x16x32_f16 v[158:161], v[64:67], v[222:225], v[158:161]
	v_mfma_f32_16x16x32_f16 v[166:169], v[64:67], v[226:229], v[166:169]
	v_mfma_f32_16x16x32_f16 v[190:193], v[68:71], v[214:217], v[190:193]
	v_mfma_f32_16x16x32_f16 v[202:205], v[68:71], v[218:221], v[202:205]
	v_mfma_f32_16x16x32_f16 v[206:209], v[68:71], v[222:225], v[206:209]
	v_mfma_f32_16x16x32_f16 v[210:213], v[68:71], v[226:229], v[210:213]
	s_setprio 0
	s_waitcnt vmcnt(6)
	s_waitcnt lgkmcnt(0)
	s_barrier
	ds_read_b128 v[214:217], v131 offset:32768
	ds_read_b128 v[218:221], v131 offset:34816
	ds_read_b128 v[222:225], v131 offset:36864
	ds_read_b128 v[226:229], v131 offset:38912
	ds_read_b128 v[64:67], v129 offset:32768
	ds_read_b128 v[68:71], v129 offset:34816
	s_add_u32 s80, s22, 0x800
	s_addc_u32 s81, s90, 0
	v_lshl_add_u64 v[198:199], s[38:39], 0, v[196:197]
	v_readfirstlane_b32 s1, v94
	s_mov_b32 m0, s1
	v_cvt_pk_f16_f32 v3, v2, v3
	global_load_lds_dwordx4 v[198:199], off
	v_cvt_pk_f16_f32 v2, v0, v1
	ds_write_b64 v100, v[2:3]
	s_setprio 1
	s_waitcnt lgkmcnt(1)
	v_mfma_f32_16x16x32_f16 v[104:107], v[64:67], v[222:225], v[104:107]
	v_mfma_f32_16x16x32_f16 v[108:111], v[68:71], v[214:217], v[108:111]
	v_mfma_f32_16x16x32_f16 v[112:115], v[68:71], v[218:221], v[112:115]
	v_mfma_f32_16x16x32_f16 v[116:119], v[68:71], v[222:225], v[116:119]
	v_mfma_f32_16x16x32_f16 v[246:249], v[64:67], v[214:217], v[78:81]
	v_mfma_f32_16x16x32_f16 v[230:233], v[64:67], v[218:221], v[230:233]
	v_mfma_f32_16x16x32_f16 v[234:237], v[64:67], v[226:229], v[234:237]
	v_mfma_f32_16x16x32_f16 v[238:241], v[68:71], v[226:229], v[238:241]
	s_setprio 0
	ds_read_b128 v[68:71], v129 offset:36864
	ds_read_b128 v[72:75], v129 offset:38912
	v_readfirstlane_b32 s92, v99
	v_lshl_add_u64 v[64:65], v[198:199], 0, s[58:59]
	s_mov_b32 m0, s92
	v_cvt_pk_f16_f32 v11, v10, v11
	global_load_lds_dwordx4 v[64:65], off
	v_cvt_pk_f16_f32 v10, v8, v9
	ds_write_b64 v100, v[10:11] offset:4096
	s_add_u32 s80, s22, 0x20800
	s_addc_u32 s81, s90, 0
	s_add_u32 s100, s22, 0x800
	s_addc_u32 s101, s90, 0
	global_load_dwordx4 v[0:3], v201, s[100:101] nt
	s_setprio 1
	s_waitcnt lgkmcnt(1)
	v_mfma_f32_16x16x32_f16 v[8:11], v[68:71], v[214:217], v[82:85]
	v_mfma_f32_16x16x32_f16 v[120:123], v[68:71], v[226:229], v[120:123]
	v_mfma_f32_16x16x32_f16 v[124:127], v[72:75], v[214:217], v[124:127]
	v_mfma_f32_16x16x32_f16 v[146:149], v[72:75], v[218:221], v[146:149]
	v_mfma_f32_16x16x32_f16 v[134:137], v[72:75], v[226:229], v[134:137]
	v_mfma_f32_16x16x32_f16 v[138:141], v[68:71], v[218:221], v[138:141]
	v_mfma_f32_16x16x32_f16 v[142:145], v[68:71], v[222:225], v[142:145]
	v_mfma_f32_16x16x32_f16 v[150:153], v[72:75], v[222:225], v[150:153]
	s_setprio 0
	ds_read_b128 v[72:75], v129 offset:40960
	ds_read_b128 v[76:79], v129 offset:43008
	v_readfirstlane_b32 s91, v101
	v_lshl_add_u64 v[68:69], v[198:199], 0, s[60:61]
	s_mov_b32 m0, s91
	v_cvt_pk_f16_f32 v15, v14, v15
	global_load_lds_dwordx4 v[68:69], off
	v_cvt_pk_f16_f32 v14, v12, v13
	ds_write_b64 v100, v[14:15] offset:8192
	s_add_u32 s80, s22, 0x40800
	s_addc_u32 s81, s90, 0
	s_add_u32 s100, s22, 0x20800
	s_addc_u32 s101, s90, 0
	global_load_dwordx4 v[64:67], v201, s[100:101] nt
	s_setprio 1
	s_waitcnt lgkmcnt(1)
	v_mfma_f32_16x16x32_f16 v[12:15], v[72:75], v[214:217], v[86:89]
	v_mfma_f32_16x16x32_f16 v[170:173], v[72:75], v[218:221], v[170:173]
	v_mfma_f32_16x16x32_f16 v[174:177], v[72:75], v[222:225], v[174:177]
	v_mfma_f32_16x16x32_f16 v[162:165], v[72:75], v[226:229], v[162:165]
	v_mfma_f32_16x16x32_f16 v[178:181], v[76:79], v[214:217], v[178:181]
	v_mfma_f32_16x16x32_f16 v[182:185], v[76:79], v[218:221], v[182:185]
	v_mfma_f32_16x16x32_f16 v[186:189], v[76:79], v[222:225], v[186:189]
	v_mfma_f32_16x16x32_f16 v[154:157], v[76:79], v[226:229], v[154:157]
	s_setprio 0
	ds_read_b128 v[76:79], v129 offset:45056
	ds_read_b128 v[80:83], v129 offset:47104
	v_readfirstlane_b32 s73, v102
	v_lshl_add_u64 v[72:73], v[198:199], 0, s[62:63]
	s_mov_b32 m0, s73
	v_cvt_pk_f16_f32 v19, v18, v19
	global_load_lds_dwordx4 v[72:73], off
	v_cvt_pk_f16_f32 v18, v16, v17
	ds_write_b64 v100, v[18:19] offset:12288
	s_add_u32 s80, s22, 0x60800
	s_addc_u32 s81, s90, 0
	s_add_u32 s100, s22, 0x40800
	s_addc_u32 s101, s90, 0
	global_load_dwordx4 v[68:71], v201, s[100:101] nt
	s_setprio 1
	s_waitcnt lgkmcnt(1)
	v_mfma_f32_16x16x32_f16 v[16:19], v[76:79], v[214:217], v[242:245]
	v_mfma_f32_16x16x32_f16 v[242:245], v[76:79], v[218:221], v[90:93]
	v_mfma_f32_16x16x32_f16 v[158:161], v[76:79], v[222:225], v[158:161]
	v_mfma_f32_16x16x32_f16 v[166:169], v[76:79], v[226:229], v[166:169]
	v_mfma_f32_16x16x32_f16 v[190:193], v[80:83], v[214:217], v[190:193]
	v_mfma_f32_16x16x32_f16 v[202:205], v[80:83], v[218:221], v[202:205]
	v_mfma_f32_16x16x32_f16 v[206:209], v[80:83], v[222:225], v[206:209]
	v_mfma_f32_16x16x32_f16 v[210:213], v[80:83], v[226:229], v[210:213]
	s_setprio 0
	ds_read_b128 v[214:217], v128 offset:32768
	ds_read_b128 v[218:221], v128 offset:34816
	ds_read_b128 v[222:225], v128 offset:36864
	ds_read_b128 v[226:229], v128 offset:38912
	ds_read_b128 v[80:83], v130 offset:32768
	ds_read_b128 v[84:87], v130 offset:34816
	v_cvt_pk_f16_f32 v23, v22, v23
	v_cvt_pk_f16_f32 v22, v20, v21
	ds_write_b64 v100, v[22:23] offset:16384
	s_add_u32 s80, s22, 0x80800
	s_addc_u32 s81, s90, 0
	s_add_u32 s100, s22, 0x60800
	s_addc_u32 s101, s90, 0
	global_load_dwordx4 v[72:75], v201, s[100:101] nt
	s_setprio 1
	s_waitcnt lgkmcnt(1)
	v_mfma_f32_16x16x32_f16 v[20:23], v[80:83], v[214:217], v[246:249]
	v_mfma_f32_16x16x32_f16 v[104:107], v[80:83], v[222:225], v[104:107]
	v_mfma_f32_16x16x32_f16 v[108:111], v[84:87], v[214:217], v[108:111]
	v_mfma_f32_16x16x32_f16 v[112:115], v[84:87], v[218:221], v[112:115]
	v_mfma_f32_16x16x32_f16 v[116:119], v[84:87], v[222:225], v[116:119]
	v_mfma_f32_16x16x32_f16 v[230:233], v[80:83], v[218:221], v[230:233]
	v_mfma_f32_16x16x32_f16 v[234:237], v[80:83], v[226:229], v[234:237]
	v_mfma_f32_16x16x32_f16 v[238:241], v[84:87], v[226:229], v[238:241]
	s_setprio 0
	ds_read_b128 v[84:87], v130 offset:36864
	ds_read_b128 v[88:91], v130 offset:38912
	v_cvt_pk_f16_f32 v27, v26, v27
	v_cvt_pk_f16_f32 v26, v24, v25
	ds_write_b64 v100, v[26:27] offset:20480
	s_add_u32 s80, s22, 0xa0800
	s_addc_u32 s81, s90, 0
	s_add_u32 s100, s22, 0x80800
	s_addc_u32 s101, s90, 0
	global_load_dwordx4 v[76:79], v201, s[100:101] nt
	s_setprio 1
	s_waitcnt lgkmcnt(1)
	v_mfma_f32_16x16x32_f16 v[24:27], v[84:87], v[214:217], v[8:11]
	v_mfma_f32_16x16x32_f16 v[120:123], v[84:87], v[226:229], v[120:123]
	v_mfma_f32_16x16x32_f16 v[124:127], v[88:91], v[214:217], v[124:127]
	v_mfma_f32_16x16x32_f16 v[146:149], v[88:91], v[218:221], v[146:149]
	v_mfma_f32_16x16x32_f16 v[134:137], v[88:91], v[226:229], v[134:137]
	v_mfma_f32_16x16x32_f16 v[138:141], v[84:87], v[218:221], v[138:141]
	v_mfma_f32_16x16x32_f16 v[142:145], v[84:87], v[222:225], v[142:145]
	v_mfma_f32_16x16x32_f16 v[150:153], v[88:91], v[222:225], v[150:153]
	s_setprio 0
	ds_read_b128 v[8:11], v130 offset:40960
	ds_read_b128 v[88:91], v130 offset:43008
	v_cvt_pk_f16_f32 v31, v30, v31
	v_cvt_pk_f16_f32 v30, v28, v29
	ds_write_b64 v100, v[30:31] offset:24576
	s_add_u32 s80, s22, 0xc0800
	s_addc_u32 s81, s90, 0
	s_add_u32 s100, s22, 0xa0800
	s_addc_u32 s101, s90, 0
	global_load_dwordx4 v[80:83], v201, s[100:101] nt
	s_setprio 1
	s_waitcnt lgkmcnt(1)
	v_mfma_f32_16x16x32_f16 v[12:15], v[8:11], v[214:217], v[12:15]
	v_mfma_f32_16x16x32_f16 v[28:31], v[8:11], v[218:221], v[170:173]
	v_mfma_f32_16x16x32_f16 v[170:173], v[8:11], v[222:225], v[174:177]
	v_mfma_f32_16x16x32_f16 v[162:165], v[8:11], v[226:229], v[162:165]
	v_mfma_f32_16x16x32_f16 v[174:177], v[88:91], v[214:217], v[178:181]
	v_mfma_f32_16x16x32_f16 v[178:181], v[88:91], v[218:221], v[182:185]
	v_mfma_f32_16x16x32_f16 v[182:185], v[88:91], v[222:225], v[186:189]
	v_mfma_f32_16x16x32_f16 v[154:157], v[88:91], v[226:229], v[154:157]
	s_setprio 0
	ds_read_b128 v[8:11], v130 offset:45056
	ds_read_b128 v[186:189], v130 offset:47104
	v_cvt_pk_f16_f32 v35, v34, v35
	v_cvt_pk_f16_f32 v34, v32, v33
	ds_write_b64 v100, v[34:35] offset:28672
	s_add_u32 s80, s22, 0xe0800
	s_addc_u32 s81, s90, 0
	s_add_u32 s100, s22, 0xc0800
	s_addc_u32 s101, s90, 0
	global_load_dwordx4 v[84:87], v201, s[100:101] nt
	s_add_u32 s100, s22, 0xe0800
	s_addc_u32 s101, s90, 0
	global_load_dwordx4 v[88:91], v201, s[100:101] nt
	s_setprio 1
	s_waitcnt lgkmcnt(1)
	v_mfma_f32_16x16x32_f16 v[16:19], v[8:11], v[214:217], v[16:19]
	v_mfma_f32_16x16x32_f16 v[32:35], v[8:11], v[218:221], v[242:245]
	v_mfma_f32_16x16x32_f16 v[158:161], v[8:11], v[222:225], v[158:161]
	v_mfma_f32_16x16x32_f16 v[166:169], v[8:11], v[226:229], v[166:169]
	v_mfma_f32_16x16x32_f16 v[190:193], v[186:189], v[214:217], v[190:193]
	v_mfma_f32_16x16x32_f16 v[202:205], v[186:189], v[218:221], v[202:205]
	v_mfma_f32_16x16x32_f16 v[206:209], v[186:189], v[222:225], v[206:209]
	v_mfma_f32_16x16x32_f16 v[186:189], v[186:189], v[226:229], v[210:213]
	s_setprio 0
	s_waitcnt vmcnt(6)
	s_waitcnt lgkmcnt(0)
	s_barrier
	s_nop 0
	ds_read_b128 v[210:213], v131
	ds_read_b128 v[214:217], v131 offset:2048
	ds_read_b128 v[218:221], v131 offset:4096
	ds_read_b128 v[222:225], v131 offset:6144
	ds_read_b128 v[8:11], v129
	ds_read_b128 v[226:229], v129 offset:2048
	s_add_u32 s80, s22, 0x900
	v_lshl_add_u64 v[92:93], s[40:41], 0, v[196:197]
	s_addc_u32 s81, s90, 0
	v_cvt_pk_f16_f32 v7, v6, v7
	s_cmp_lg_u32 s2, 0
	s_cbranch_scc1 .Lres_skip_0
	s_add_u32 m0, s0, 0x18000
	s_nop 0
	global_load_lds_dwordx4 v[92:93], off
.Lres_skip_0:
	v_cvt_pk_f16_f32 v6, v4, v5
	ds_write_b64 v100, v[6:7] offset:32768
	s_setprio 1
	s_waitcnt lgkmcnt(1)
	v_mfma_f32_16x16x32_f16 v[20:23], v[8:11], v[210:213], v[20:23]
	v_mfma_f32_16x16x32_f16 v[104:107], v[8:11], v[218:221], v[104:107]
	v_mfma_f32_16x16x32_f16 v[108:111], v[226:229], v[210:213], v[108:111]
	v_mfma_f32_16x16x32_f16 v[112:115], v[226:229], v[214:217], v[112:115]
	v_mfma_f32_16x16x32_f16 v[116:119], v[226:229], v[218:221], v[116:119]
	v_mfma_f32_16x16x32_f16 v[230:233], v[8:11], v[214:217], v[230:233]
	v_mfma_f32_16x16x32_f16 v[234:237], v[8:11], v[222:225], v[234:237]
	v_mfma_f32_16x16x32_f16 v[226:229], v[226:229], v[222:225], v[238:241]
	s_setprio 0
	s_nop 1
	ds_read_b128 v[238:241], v129 offset:4096
	ds_read_b128 v[242:245], v129 offset:6144
	s_cmp_lg_u32 s2, 0
	s_cbranch_scc1 .Lres_skip_1
	s_add_u32 m0, s72, 0x18000
	s_nop 0
	v_lshl_add_u64 v[8:9], v[92:93], 0, s[58:59]
	global_load_lds_dwordx4 v[8:9], off
.Lres_skip_1:
	v_cvt_pk_f16_f32 v9, v42, v43
	v_cvt_pk_f16_f32 v8, v40, v41
	ds_write_b64 v100, v[8:9] offset:36864
	s_add_u32 s80, s22, 0x20900
	s_addc_u32 s81, s90, 0
	s_add_u32 s100, s22, 0x900
	s_addc_u32 s101, s90, 0
	global_load_dwordx4 v[4:7], v201, s[100:101] nt
	s_setprio 1
	s_waitcnt lgkmcnt(1)
	v_mfma_f32_16x16x32_f16 v[24:27], v[238:241], v[210:213], v[24:27]
	v_mfma_f32_16x16x32_f16 v[120:123], v[238:241], v[222:225], v[120:123]
	v_mfma_f32_16x16x32_f16 v[124:127], v[242:245], v[210:213], v[124:127]
	v_mfma_f32_16x16x32_f16 v[146:149], v[242:245], v[214:217], v[146:149]
	v_mfma_f32_16x16x32_f16 v[134:137], v[242:245], v[222:225], v[134:137]
	v_mfma_f32_16x16x32_f16 v[138:141], v[238:241], v[214:217], v[138:141]
	v_mfma_f32_16x16x32_f16 v[142:145], v[238:241], v[218:221], v[142:145]
	v_mfma_f32_16x16x32_f16 v[150:153], v[242:245], v[218:221], v[150:153]
	s_setprio 0
	ds_read_b128 v[238:241], v129 offset:8192
	ds_read_b128 v[242:245], v129 offset:10240
	s_cmp_lg_u32 s2, 0
	s_cbranch_scc1 .Lres_skip_2
	s_add_u32 m0, s71, 0x18000
	s_nop 0
	v_lshl_add_u64 v[40:41], v[92:93], 0, s[60:61]
	global_load_lds_dwordx4 v[40:41], off
.Lres_skip_2:
	v_cvt_pk_f16_f32 v41, v46, v47
	v_cvt_pk_f16_f32 v40, v44, v45
	ds_write_b64 v100, v[40:41] offset:40960
	s_add_u32 s80, s22, 0x40900
	s_addc_u32 s81, s90, 0
	s_add_u32 s100, s22, 0x20900
	s_addc_u32 s101, s90, 0
	global_load_dwordx4 v[8:11], v201, s[100:101] nt
	s_setprio 1
	s_waitcnt lgkmcnt(1)
	v_mfma_f32_16x16x32_f16 v[12:15], v[238:241], v[210:213], v[12:15]
	v_mfma_f32_16x16x32_f16 v[28:31], v[238:241], v[214:217], v[28:31]
	v_mfma_f32_16x16x32_f16 v[170:173], v[238:241], v[218:221], v[170:173]
	v_mfma_f32_16x16x32_f16 v[162:165], v[238:241], v[222:225], v[162:165]
	v_mfma_f32_16x16x32_f16 v[174:177], v[242:245], v[210:213], v[174:177]
	v_mfma_f32_16x16x32_f16 v[178:181], v[242:245], v[214:217], v[178:181]
	v_mfma_f32_16x16x32_f16 v[182:185], v[242:245], v[218:221], v[182:185]
	v_mfma_f32_16x16x32_f16 v[154:157], v[242:245], v[222:225], v[154:157]
	s_setprio 0
	ds_read_b128 v[238:241], v129 offset:12288
	ds_read_b128 v[242:245], v129 offset:14336
	s_cmp_lg_u32 s2, 0
	s_cbranch_scc1 .Lres_skip_3
	s_add_u32 m0, s70, 0x18000
	s_nop 0
	v_lshl_add_u64 v[44:45], v[92:93], 0, s[62:63]
	global_load_lds_dwordx4 v[44:45], off
.Lres_skip_3:
	v_cvt_pk_f16_f32 v45, v50, v51
	v_cvt_pk_f16_f32 v44, v48, v49
	ds_write_b64 v100, v[44:45] offset:45056
	s_add_u32 s70, s22, 0x60900
	s_addc_u32 s71, s90, 0
	s_add_u32 s100, s22, 0x40900
	s_addc_u32 s101, s90, 0
	global_load_dwordx4 v[40:43], v201, s[100:101] nt
	s_setprio 1
	s_waitcnt lgkmcnt(1)
	v_mfma_f32_16x16x32_f16 v[16:19], v[238:241], v[210:213], v[16:19]
	v_mfma_f32_16x16x32_f16 v[32:35], v[238:241], v[214:217], v[32:35]
	v_mfma_f32_16x16x32_f16 v[158:161], v[238:241], v[218:221], v[158:161]
	v_mfma_f32_16x16x32_f16 v[166:169], v[238:241], v[222:225], v[166:169]
	v_mfma_f32_16x16x32_f16 v[190:193], v[242:245], v[210:213], v[190:193]
	v_mfma_f32_16x16x32_f16 v[202:205], v[242:245], v[214:217], v[202:205]
	v_mfma_f32_16x16x32_f16 v[206:209], v[242:245], v[218:221], v[206:209]
	v_mfma_f32_16x16x32_f16 v[186:189], v[242:245], v[222:225], v[186:189]
	s_setprio 0
	ds_read_b128 v[210:213], v128
	ds_read_b128 v[214:217], v128 offset:2048
	ds_read_b128 v[218:221], v128 offset:4096
	ds_read_b128 v[222:225], v128 offset:6144
	ds_read_b128 v[238:241], v130
	ds_read_b128 v[242:245], v130 offset:2048
	v_cvt_pk_f16_f32 v49, v54, v55
	v_cvt_pk_f16_f32 v48, v52, v53
	ds_write_b64 v100, v[48:49] offset:49152
	s_add_u32 s70, s22, 0x80900
	s_addc_u32 s71, s90, 0
	s_add_u32 s100, s22, 0x60900
	s_addc_u32 s101, s90, 0
	global_load_dwordx4 v[44:47], v201, s[100:101] nt
	s_setprio 1
	s_waitcnt lgkmcnt(1)
	v_mfma_f32_16x16x32_f16 v[20:23], v[238:241], v[210:213], v[20:23]
	v_mfma_f32_16x16x32_f16 v[104:107], v[238:241], v[218:221], v[104:107]
	v_mfma_f32_16x16x32_f16 v[108:111], v[242:245], v[210:213], v[108:111]
	v_mfma_f32_16x16x32_f16 v[112:115], v[242:245], v[214:217], v[112:115]
	v_mfma_f32_16x16x32_f16 v[116:119], v[242:245], v[218:221], v[116:119]
	v_mfma_f32_16x16x32_f16 v[230:233], v[238:241], v[214:217], v[230:233]
	v_mfma_f32_16x16x32_f16 v[234:237], v[238:241], v[222:225], v[234:237]
	v_mfma_f32_16x16x32_f16 v[226:229], v[242:245], v[222:225], v[226:229]
	s_setprio 0
	ds_read_b128 v[238:241], v130 offset:4096
	ds_read_b128 v[242:245], v130 offset:6144
	v_cvt_pk_f16_f32 v53, v58, v59
	v_cvt_pk_f16_f32 v52, v56, v57
	ds_write_b64 v100, v[52:53] offset:53248
	s_add_u32 s70, s22, 0xa0900
	s_addc_u32 s71, s90, 0
	s_add_u32 s100, s22, 0x80900
	s_addc_u32 s101, s90, 0
	global_load_dwordx4 v[48:51], v201, s[100:101] nt
	s_setprio 1
	s_waitcnt lgkmcnt(1)
	v_mfma_f32_16x16x32_f16 v[24:27], v[238:241], v[210:213], v[24:27]
	v_mfma_f32_16x16x32_f16 v[120:123], v[238:241], v[222:225], v[120:123]
	v_mfma_f32_16x16x32_f16 v[124:127], v[242:245], v[210:213], v[124:127]
	v_mfma_f32_16x16x32_f16 v[146:149], v[242:245], v[214:217], v[146:149]
	v_mfma_f32_16x16x32_f16 v[134:137], v[242:245], v[222:225], v[134:137]
	v_mfma_f32_16x16x32_f16 v[138:141], v[238:241], v[214:217], v[138:141]
	v_mfma_f32_16x16x32_f16 v[142:145], v[238:241], v[218:221], v[142:145]
	v_mfma_f32_16x16x32_f16 v[150:153], v[242:245], v[218:221], v[150:153]
	s_setprio 0
	ds_read_b128 v[238:241], v130 offset:8192
	ds_read_b128 v[242:245], v130 offset:10240
	v_cvt_pk_f16_f32 v57, v62, v63
	v_cvt_pk_f16_f32 v56, v60, v61
	ds_write_b64 v100, v[56:57] offset:57344
	s_add_u32 s70, s22, 0xc0900
	s_addc_u32 s71, s90, 0
	s_add_u32 s100, s22, 0xa0900
	s_addc_u32 s101, s90, 0
	global_load_dwordx4 v[52:55], v201, s[100:101] nt
	s_setprio 1
	s_waitcnt lgkmcnt(1)
	v_mfma_f32_16x16x32_f16 v[28:31], v[238:241], v[214:217], v[28:31]
	v_mfma_f32_16x16x32_f16 v[246:249], v[238:241], v[210:213], v[12:15]
	v_mfma_f32_16x16x32_f16 v[170:173], v[238:241], v[218:221], v[170:173]
	v_mfma_f32_16x16x32_f16 v[162:165], v[238:241], v[222:225], v[162:165]
	v_mfma_f32_16x16x32_f16 v[174:177], v[242:245], v[210:213], v[174:177]
	v_mfma_f32_16x16x32_f16 v[178:181], v[242:245], v[214:217], v[178:181]
	v_mfma_f32_16x16x32_f16 v[182:185], v[242:245], v[218:221], v[182:185]
	v_mfma_f32_16x16x32_f16 v[154:157], v[242:245], v[222:225], v[154:157]
	s_setprio 0
	ds_read_b128 v[12:15], v130 offset:12288
	ds_read_b128 v[238:241], v130 offset:14336
	v_cvt_pk_f16_f32 v39, v38, v39
	v_cvt_pk_f16_f32 v38, v36, v37
	ds_write_b64 v100, v[38:39] offset:61440
	s_add_u32 s70, s22, 0xe0900
	s_addc_u32 s71, s90, 0
	s_add_u32 s100, s22, 0xc0900
	s_addc_u32 s101, s90, 0
	global_load_dwordx4 v[56:59], v201, s[100:101] nt
	s_add_u32 s100, s22, 0xe0900
	s_addc_u32 s101, s90, 0
	global_load_dwordx4 v[60:63], v201, s[100:101] nt
	s_setprio 1
	s_waitcnt lgkmcnt(1)
	v_mfma_f32_16x16x32_f16 v[36:39], v[12:15], v[210:213], v[16:19]
	v_mfma_f32_16x16x32_f16 v[32:35], v[12:15], v[214:217], v[32:35]
	v_mfma_f32_16x16x32_f16 v[158:161], v[12:15], v[218:221], v[158:161]
	v_mfma_f32_16x16x32_f16 v[166:169], v[12:15], v[222:225], v[166:169]
	v_mfma_f32_16x16x32_f16 v[190:193], v[238:241], v[210:213], v[190:193]
	v_mfma_f32_16x16x32_f16 v[202:205], v[238:241], v[214:217], v[202:205]
	v_mfma_f32_16x16x32_f16 v[206:209], v[238:241], v[218:221], v[206:209]
	v_mfma_f32_16x16x32_f16 v[186:189], v[238:241], v[222:225], v[186:189]
	s_setprio 0
	s_waitcnt vmcnt(6)
	s_waitcnt lgkmcnt(0)
	s_barrier
	v_add_u32_e32 v250, 0x20000, v129
	v_add_u32_e32 v251, 0x20000, v130
	ds_read_b128 v[210:213], v131 offset:32768
	ds_read_b128 v[214:217], v131 offset:34816
	ds_read_b128 v[218:221], v131 offset:36864
	ds_read_b128 v[222:225], v131 offset:38912
	ds_read_b128 v[12:15], v250
	ds_read_b128 v[16:19], v250 offset:2048
	s_add_u32 s70, s22, 0xa00
	v_lshl_add_u64 v[92:93], s[42:43], 0, v[196:197]
	s_addc_u32 s71, s90, 0
	s_mov_b32 m0, s1
	v_cvt_pk_f16_f32 v3, v2, v3
	global_load_lds_dwordx4 v[92:93], off
	v_cvt_pk_f16_f32 v2, v0, v1
	ds_write_b64 v100, v[2:3]
	s_setprio 1
	s_waitcnt lgkmcnt(1)
	v_mfma_f32_16x16x32_f16 v[104:107], v[12:15], v[218:221], v[104:107]
	v_mfma_f32_16x16x32_f16 v[108:111], v[16:19], v[210:213], v[108:111]
	v_mfma_f32_16x16x32_f16 v[112:115], v[16:19], v[214:217], v[112:115]
	v_mfma_f32_16x16x32_f16 v[116:119], v[16:19], v[218:221], v[116:119]
	v_mfma_f32_16x16x32_f16 v[238:241], v[12:15], v[210:213], v[20:23]
	v_mfma_f32_16x16x32_f16 v[230:233], v[12:15], v[214:217], v[230:233]
	v_mfma_f32_16x16x32_f16 v[234:237], v[12:15], v[222:225], v[234:237]
	v_mfma_f32_16x16x32_f16 v[226:229], v[16:19], v[222:225], v[226:229]
	s_setprio 0
	ds_read_b128 v[16:19], v250 offset:4096
	ds_read_b128 v[20:23], v250 offset:6144
	s_mov_b32 m0, s92
	v_lshl_add_u64 v[12:13], v[92:93], 0, s[58:59]
	global_load_lds_dwordx4 v[12:13], off
	v_cvt_pk_f16_f32 v13, v66, v67
	v_cvt_pk_f16_f32 v12, v64, v65
	ds_write_b64 v100, v[12:13] offset:4096
	s_add_u32 s0, s22, 0x20a00
	s_addc_u32 s1, s90, 0
	s_add_u32 s100, s22, 0xa00
	s_addc_u32 s101, s90, 0
	global_load_dwordx4 v[0:3], v201, s[100:101] nt
	s_setprio 1
	s_waitcnt lgkmcnt(1)
	v_mfma_f32_16x16x32_f16 v[64:67], v[16:19], v[210:213], v[24:27]
	v_mfma_f32_16x16x32_f16 v[120:123], v[16:19], v[222:225], v[120:123]
	v_mfma_f32_16x16x32_f16 v[124:127], v[20:23], v[210:213], v[124:127]
	v_mfma_f32_16x16x32_f16 v[146:149], v[20:23], v[214:217], v[146:149]
	v_mfma_f32_16x16x32_f16 v[134:137], v[20:23], v[222:225], v[134:137]
	v_mfma_f32_16x16x32_f16 v[138:141], v[16:19], v[214:217], v[138:141]
	v_mfma_f32_16x16x32_f16 v[142:145], v[16:19], v[218:221], v[142:145]
	v_mfma_f32_16x16x32_f16 v[150:153], v[20:23], v[218:221], v[150:153]
	s_setprio 0
	ds_read_b128 v[20:23], v250 offset:8192
	ds_read_b128 v[24:27], v250 offset:10240
	s_mov_b32 m0, s91
	v_lshl_add_u64 v[16:17], v[92:93], 0, s[60:61]
	global_load_lds_dwordx4 v[16:17], off
	v_cvt_pk_f16_f32 v17, v70, v71
	v_cvt_pk_f16_f32 v16, v68, v69
	ds_write_b64 v100, v[16:17] offset:8192
	s_add_u32 s0, s22, 0x40a00
	s_addc_u32 s1, s90, 0
	s_add_u32 s100, s22, 0x20a00
	s_addc_u32 s101, s90, 0
	global_load_dwordx4 v[12:15], v201, s[100:101] nt
	s_setprio 1
	s_waitcnt lgkmcnt(1)
	v_mfma_f32_16x16x32_f16 v[68:71], v[20:23], v[210:213], v[246:249]
	v_mfma_f32_16x16x32_f16 v[242:245], v[20:23], v[214:217], v[28:31]
	v_mfma_f32_16x16x32_f16 v[170:173], v[20:23], v[218:221], v[170:173]
	v_mfma_f32_16x16x32_f16 v[162:165], v[20:23], v[222:225], v[162:165]
	v_mfma_f32_16x16x32_f16 v[174:177], v[24:27], v[210:213], v[174:177]
	v_mfma_f32_16x16x32_f16 v[178:181], v[24:27], v[214:217], v[178:181]
	v_mfma_f32_16x16x32_f16 v[182:185], v[24:27], v[218:221], v[182:185]
	v_mfma_f32_16x16x32_f16 v[154:157], v[24:27], v[222:225], v[154:157]
	s_setprio 0
	ds_read_b128 v[24:27], v250 offset:12288
	ds_read_b128 v[28:31], v250 offset:14336
	s_mov_b32 m0, s73
	v_lshl_add_u64 v[20:21], v[92:93], 0, s[62:63]
	global_load_lds_dwordx4 v[20:21], off
	v_cvt_pk_f16_f32 v21, v74, v75
	v_cvt_pk_f16_f32 v20, v72, v73
	ds_write_b64 v100, v[20:21] offset:12288
	s_add_u32 s0, s22, 0x60a00
	s_addc_u32 s1, s90, 0
	s_add_u32 s100, s22, 0x40a00
	s_addc_u32 s101, s90, 0
	global_load_dwordx4 v[16:19], v201, s[100:101] nt
	s_setprio 1
	s_waitcnt lgkmcnt(1)
	v_mfma_f32_16x16x32_f16 v[72:75], v[24:27], v[210:213], v[36:39]
	v_mfma_f32_16x16x32_f16 v[246:249], v[24:27], v[214:217], v[32:35]
	v_mfma_f32_16x16x32_f16 v[158:161], v[24:27], v[218:221], v[158:161]
	v_mfma_f32_16x16x32_f16 v[166:169], v[24:27], v[222:225], v[166:169]
	v_mfma_f32_16x16x32_f16 v[190:193], v[28:31], v[210:213], v[190:193]
	v_mfma_f32_16x16x32_f16 v[202:205], v[28:31], v[214:217], v[202:205]
	v_mfma_f32_16x16x32_f16 v[206:209], v[28:31], v[218:221], v[206:209]
	v_mfma_f32_16x16x32_f16 v[186:189], v[28:31], v[222:225], v[186:189]
	s_setprio 0
	ds_read_b128 v[210:213], v128 offset:32768
	ds_read_b128 v[214:217], v128 offset:34816
	ds_read_b128 v[218:221], v128 offset:36864
	ds_read_b128 v[222:225], v128 offset:38912
	ds_read_b128 v[28:31], v251
	ds_read_b128 v[32:35], v251 offset:2048
	v_cvt_pk_f16_f32 v25, v78, v79
	v_cvt_pk_f16_f32 v24, v76, v77
	ds_write_b64 v100, v[24:25] offset:16384
	s_add_u32 s0, s22, 0x80a00
	s_addc_u32 s1, s90, 0
	s_add_u32 s100, s22, 0x60a00
	s_addc_u32 s101, s90, 0
	global_load_dwordx4 v[20:23], v201, s[100:101] nt
	s_setprio 1
	s_waitcnt lgkmcnt(1)
	v_mfma_f32_16x16x32_f16 v[76:79], v[28:31], v[210:213], v[238:241]
	v_mfma_f32_16x16x32_f16 v[104:107], v[28:31], v[218:221], v[104:107]
	v_mfma_f32_16x16x32_f16 v[108:111], v[32:35], v[210:213], v[108:111]
	v_mfma_f32_16x16x32_f16 v[112:115], v[32:35], v[214:217], v[112:115]
	v_mfma_f32_16x16x32_f16 v[116:119], v[32:35], v[218:221], v[116:119]
	v_mfma_f32_16x16x32_f16 v[230:233], v[28:31], v[214:217], v[230:233]
	v_mfma_f32_16x16x32_f16 v[234:237], v[28:31], v[222:225], v[234:237]
	v_mfma_f32_16x16x32_f16 v[226:229], v[32:35], v[222:225], v[226:229]
	s_setprio 0
	ds_read_b128 v[32:35], v251 offset:4096
	ds_read_b128 v[36:39], v251 offset:6144
	v_cvt_pk_f16_f32 v29, v82, v83
	v_cvt_pk_f16_f32 v28, v80, v81
	ds_write_b64 v100, v[28:29] offset:20480
	s_add_u32 s0, s22, 0xa0a00
	s_addc_u32 s1, s90, 0
	s_add_u32 s100, s22, 0x80a00
	s_addc_u32 s101, s90, 0
	global_load_dwordx4 v[24:27], v201, s[100:101] nt
	s_setprio 1
	s_waitcnt lgkmcnt(1)
	v_mfma_f32_16x16x32_f16 v[80:83], v[32:35], v[210:213], v[64:67]
	v_mfma_f32_16x16x32_f16 v[120:123], v[32:35], v[222:225], v[120:123]
	v_mfma_f32_16x16x32_f16 v[124:127], v[36:39], v[210:213], v[124:127]
	v_mfma_f32_16x16x32_f16 v[146:149], v[36:39], v[214:217], v[146:149]
	v_mfma_f32_16x16x32_f16 v[134:137], v[36:39], v[222:225], v[134:137]
	v_mfma_f32_16x16x32_f16 v[138:141], v[32:35], v[214:217], v[138:141]
	v_mfma_f32_16x16x32_f16 v[142:145], v[32:35], v[218:221], v[142:145]
	v_mfma_f32_16x16x32_f16 v[150:153], v[36:39], v[218:221], v[150:153]
	s_setprio 0
	ds_read_b128 v[36:39], v251 offset:8192
	ds_read_b128 v[64:67], v251 offset:10240
	v_cvt_pk_f16_f32 v33, v86, v87
	v_cvt_pk_f16_f32 v32, v84, v85
	ds_write_b64 v100, v[32:33] offset:24576
	s_add_u32 s0, s22, 0xc0a00
	s_addc_u32 s1, s90, 0
	s_add_u32 s100, s22, 0xa0a00
	s_addc_u32 s101, s90, 0
	global_load_dwordx4 v[28:31], v201, s[100:101] nt
	s_setprio 1
	s_waitcnt lgkmcnt(1)
	v_mfma_f32_16x16x32_f16 v[68:71], v[36:39], v[210:213], v[68:71]
	v_mfma_f32_16x16x32_f16 v[84:87], v[36:39], v[214:217], v[242:245]
	v_mfma_f32_16x16x32_f16 v[170:173], v[36:39], v[218:221], v[170:173]
	v_mfma_f32_16x16x32_f16 v[162:165], v[36:39], v[222:225], v[162:165]
	v_mfma_f32_16x16x32_f16 v[174:177], v[64:67], v[210:213], v[174:177]
	v_mfma_f32_16x16x32_f16 v[178:181], v[64:67], v[214:217], v[178:181]
	v_mfma_f32_16x16x32_f16 v[182:185], v[64:67], v[218:221], v[182:185]
	v_mfma_f32_16x16x32_f16 v[154:157], v[64:67], v[222:225], v[154:157]
	s_setprio 0
	ds_read_b128 v[64:67], v251 offset:12288
	ds_read_b128 v[238:241], v251 offset:14336
	v_cvt_pk_f16_f32 v37, v90, v91
	v_cvt_pk_f16_f32 v36, v88, v89
	ds_write_b64 v100, v[36:37] offset:28672
	s_add_u32 s0, s22, 0xe0a00
	s_addc_u32 s1, s90, 0
	s_add_u32 s100, s22, 0xc0a00
	s_addc_u32 s101, s90, 0
	global_load_dwordx4 v[32:35], v201, s[100:101] nt
	s_add_u32 s100, s22, 0xe0a00
	s_addc_u32 s101, s90, 0
	global_load_dwordx4 v[36:39], v201, s[100:101] nt
	s_setprio 1
	s_waitcnt lgkmcnt(1)
	v_mfma_f32_16x16x32_f16 v[72:75], v[64:67], v[210:213], v[72:75]
	v_mfma_f32_16x16x32_f16 v[88:91], v[64:67], v[214:217], v[246:249]
	v_mfma_f32_16x16x32_f16 v[158:161], v[64:67], v[218:221], v[158:161]
	v_mfma_f32_16x16x32_f16 v[166:169], v[64:67], v[222:225], v[166:169]
	v_mfma_f32_16x16x32_f16 v[190:193], v[238:241], v[210:213], v[190:193]
	v_mfma_f32_16x16x32_f16 v[202:205], v[238:241], v[214:217], v[202:205]
	v_mfma_f32_16x16x32_f16 v[206:209], v[238:241], v[218:221], v[206:209]
	v_mfma_f32_16x16x32_f16 v[186:189], v[238:241], v[222:225], v[186:189]
	s_setprio 0
	s_waitcnt vmcnt(6)
	s_waitcnt lgkmcnt(0)
	s_barrier
	ds_read_b128 v[210:213], v131
	ds_read_b128 v[214:217], v131 offset:2048
	ds_read_b128 v[218:221], v131 offset:4096
	ds_read_b128 v[222:225], v131 offset:6144
	ds_read_b128 v[64:67], v129
	ds_read_b128 v[238:241], v129 offset:2048
	s_add_u32 s70, s22, 0xb00
	v_lshl_add_u64 v[92:93], s[44:45], 0, v[196:197]
	s_addc_u32 s71, s90, 0
	v_readfirstlane_b32 s0, v95
	s_mov_b32 m0, s0
	v_cvt_pk_f16_f32 v7, v6, v7
	global_load_lds_dwordx4 v[92:93], off
	v_cvt_pk_f16_f32 v6, v4, v5
	ds_write_b64 v100, v[6:7] offset:32768
	s_setprio 1
	s_waitcnt lgkmcnt(1)
	v_mfma_f32_16x16x32_f16 v[76:79], v[64:67], v[210:213], v[76:79]
	v_mfma_f32_16x16x32_f16 v[104:107], v[64:67], v[218:221], v[104:107]
	v_mfma_f32_16x16x32_f16 v[108:111], v[238:241], v[210:213], v[108:111]
	v_mfma_f32_16x16x32_f16 v[112:115], v[238:241], v[214:217], v[112:115]
	v_mfma_f32_16x16x32_f16 v[116:119], v[238:241], v[218:221], v[116:119]
	v_mfma_f32_16x16x32_f16 v[230:233], v[64:67], v[214:217], v[230:233]
	v_mfma_f32_16x16x32_f16 v[234:237], v[64:67], v[222:225], v[234:237]
	v_mfma_f32_16x16x32_f16 v[226:229], v[238:241], v[222:225], v[226:229]
	s_setprio 0
	ds_read_b128 v[238:241], v129 offset:4096
	ds_read_b128 v[242:245], v129 offset:6144
	v_readfirstlane_b32 s72, v96
	v_lshl_add_u64 v[64:65], v[92:93], 0, s[58:59]
	s_mov_b32 m0, s72
	v_cvt_pk_f16_f32 v11, v10, v11
	global_load_lds_dwordx4 v[64:65], off
	v_cvt_pk_f16_f32 v10, v8, v9
	ds_write_b64 v100, v[10:11] offset:36864
	s_add_u32 s70, s22, 0x20b00
	s_addc_u32 s71, s90, 0
	s_add_u32 s100, s22, 0xb00
	s_addc_u32 s101, s90, 0
	global_load_dwordx4 v[4:7], v201, s[100:101] nt
	s_setprio 1
	s_waitcnt lgkmcnt(1)
	v_mfma_f32_16x16x32_f16 v[8:11], v[238:241], v[210:213], v[80:83]
	v_mfma_f32_16x16x32_f16 v[80:83], v[238:241], v[214:217], v[138:141]
	v_mfma_f32_16x16x32_f16 v[138:141], v[238:241], v[218:221], v[142:145]
	v_mfma_f32_16x16x32_f16 v[120:123], v[238:241], v[222:225], v[120:123]
	v_mfma_f32_16x16x32_f16 v[124:127], v[242:245], v[210:213], v[124:127]
	v_mfma_f32_16x16x32_f16 v[142:145], v[242:245], v[214:217], v[146:149]
	v_mfma_f32_16x16x32_f16 v[146:149], v[242:245], v[218:221], v[150:153]
	v_mfma_f32_16x16x32_f16 v[134:137], v[242:245], v[222:225], v[134:137]
	s_setprio 0
	s_nop 0
	ds_read_b128 v[150:153], v129 offset:8192
	ds_read_b128 v[238:241], v129 offset:10240
	v_readfirstlane_b32 s71, v97
	v_lshl_add_u64 v[198:199], v[92:93], 0, s[60:61]
	s_mov_b32 m0, s71
	v_cvt_pk_f16_f32 v43, v42, v43
	global_load_lds_dwordx4 v[198:199], off
	v_cvt_pk_f16_f32 v42, v40, v41
	ds_write_b64 v100, v[42:43] offset:40960
	s_add_u32 s80, s22, 0x40b00
	s_addc_u32 s81, s90, 0
	s_add_u32 s100, s22, 0x20b00
	s_addc_u32 s101, s90, 0
	global_load_dwordx4 v[64:67], v201, s[100:101] nt
	s_setprio 1
	s_waitcnt lgkmcnt(1)
	v_mfma_f32_16x16x32_f16 v[68:71], v[150:153], v[210:213], v[68:71]
	v_mfma_f32_16x16x32_f16 v[84:87], v[150:153], v[214:217], v[84:87]
	v_mfma_f32_16x16x32_f16 v[170:173], v[150:153], v[218:221], v[170:173]
	v_mfma_f32_16x16x32_f16 v[150:153], v[150:153], v[222:225], v[162:165]
	v_mfma_f32_16x16x32_f16 v[162:165], v[238:241], v[210:213], v[174:177]
	v_mfma_f32_16x16x32_f16 v[174:177], v[238:241], v[214:217], v[178:181]
	v_mfma_f32_16x16x32_f16 v[178:181], v[238:241], v[218:221], v[182:185]
	v_mfma_f32_16x16x32_f16 v[154:157], v[238:241], v[222:225], v[154:157]
	s_setprio 0
	s_nop 0
	ds_read_b128 v[182:185], v129 offset:12288
	ds_read_b128 v[238:241], v129 offset:14336
	v_readfirstlane_b32 s70, v98
	v_lshl_add_u64 v[92:93], v[92:93], 0, s[62:63]
	s_mov_b32 m0, s70
	v_cvt_pk_f16_f32 v47, v46, v47
	global_load_lds_dwordx4 v[92:93], off
	v_cvt_pk_f16_f32 v46, v44, v45
	ds_write_b64 v100, v[46:47] offset:45056
	s_add_u32 s80, s22, 0x60b00
	s_addc_u32 s81, s90, 0
	s_add_u32 s100, s22, 0x40b00
	s_addc_u32 s101, s90, 0
	global_load_dwordx4 v[40:43], v201, s[100:101] nt
	s_setprio 1
	s_waitcnt lgkmcnt(1)
	v_mfma_f32_16x16x32_f16 v[72:75], v[182:185], v[210:213], v[72:75]
	v_mfma_f32_16x16x32_f16 v[88:91], v[182:185], v[214:217], v[88:91]
	v_mfma_f32_16x16x32_f16 v[158:161], v[182:185], v[218:221], v[158:161]
	v_mfma_f32_16x16x32_f16 v[166:169], v[182:185], v[222:225], v[166:169]
	v_mfma_f32_16x16x32_f16 v[182:185], v[238:241], v[210:213], v[190:193]
	v_mfma_f32_16x16x32_f16 v[190:193], v[238:241], v[214:217], v[202:205]
	v_mfma_f32_16x16x32_f16 v[202:205], v[238:241], v[218:221], v[206:209]
	v_mfma_f32_16x16x32_f16 v[186:189], v[238:241], v[222:225], v[186:189]
	s_setprio 0
	s_nop 0
	ds_read_b128 v[206:209], v128
	ds_read_b128 v[210:213], v128 offset:2048
	ds_read_b128 v[214:217], v128 offset:4096
	ds_read_b128 v[218:221], v128 offset:6144
	ds_read_b128 v[222:225], v130
	ds_read_b128 v[238:241], v130 offset:2048
	v_cvt_pk_f16_f32 v51, v50, v51
	v_cvt_pk_f16_f32 v50, v48, v49
	ds_write_b64 v100, v[50:51] offset:49152
	s_add_u32 s80, s22, 0x80b00
	s_addc_u32 s81, s90, 0
	s_add_u32 s100, s22, 0x60b00
	s_addc_u32 s101, s90, 0
	global_load_dwordx4 v[44:47], v201, s[100:101] nt
	s_setprio 1
	s_waitcnt lgkmcnt(1)
	v_mfma_f32_16x16x32_f16 v[76:79], v[222:225], v[206:209], v[76:79]
	v_mfma_f32_16x16x32_f16 v[104:107], v[222:225], v[214:217], v[104:107]
	v_mfma_f32_16x16x32_f16 v[108:111], v[238:241], v[206:209], v[108:111]
	v_mfma_f32_16x16x32_f16 v[112:115], v[238:241], v[210:213], v[112:115]
	v_mfma_f32_16x16x32_f16 v[116:119], v[238:241], v[214:217], v[116:119]
	v_mfma_f32_16x16x32_f16 v[230:233], v[222:225], v[210:213], v[230:233]
	v_mfma_f32_16x16x32_f16 v[222:225], v[222:225], v[218:221], v[234:237]
	v_mfma_f32_16x16x32_f16 v[226:229], v[238:241], v[218:221], v[226:229]
	s_setprio 0
	s_nop 0
	ds_read_b128 v[234:237], v130 offset:4096
	ds_read_b128 v[238:241], v130 offset:6144
	v_cvt_pk_f16_f32 v55, v54, v55
	v_cvt_pk_f16_f32 v54, v52, v53
	ds_write_b64 v100, v[54:55] offset:53248
	s_add_u32 s80, s22, 0xa0b00
	s_addc_u32 s81, s90, 0
	s_add_u32 s100, s22, 0x80b00
	s_addc_u32 s101, s90, 0
	global_load_dwordx4 v[48:51], v201, s[100:101] nt
	s_setprio 1
	s_waitcnt lgkmcnt(1)
	v_mfma_f32_16x16x32_f16 v[80:83], v[234:237], v[210:213], v[80:83]
	v_mfma_f32_16x16x32_f16 v[120:123], v[234:237], v[218:221], v[120:123]
	v_mfma_f32_16x16x32_f16 v[124:127], v[238:241], v[206:209], v[124:127]
	v_mfma_f32_16x16x32_f16 v[146:149], v[238:241], v[214:217], v[146:149]
	v_mfma_f32_16x16x32_f16 v[134:137], v[238:241], v[218:221], v[134:137]
	v_mfma_f32_16x16x32_f16 v[242:245], v[234:237], v[206:209], v[8:11]
	v_mfma_f32_16x16x32_f16 v[138:141], v[234:237], v[214:217], v[138:141]
	v_mfma_f32_16x16x32_f16 v[142:145], v[238:241], v[210:213], v[142:145]
	s_setprio 0
	ds_read_b128 v[8:11], v130 offset:8192
	ds_read_b128 v[234:237], v130 offset:10240
	v_cvt_pk_f16_f32 v59, v58, v59
	v_cvt_pk_f16_f32 v58, v56, v57
	ds_write_b64 v100, v[58:59] offset:57344
	s_add_u32 s80, s22, 0xc0b00
	s_addc_u32 s81, s90, 0
	s_add_u32 s100, s22, 0xa0b00
	s_addc_u32 s101, s90, 0
	global_load_dwordx4 v[52:55], v201, s[100:101] nt
	s_setprio 1
	s_waitcnt lgkmcnt(1)
	v_mfma_f32_16x16x32_f16 v[84:87], v[8:11], v[210:213], v[84:87]
	v_mfma_f32_16x16x32_f16 v[238:241], v[8:11], v[206:209], v[68:71]
	v_mfma_f32_16x16x32_f16 v[170:173], v[8:11], v[214:217], v[170:173]
	v_mfma_f32_16x16x32_f16 v[150:153], v[8:11], v[218:221], v[150:153]
	v_mfma_f32_16x16x32_f16 v[162:165], v[234:237], v[206:209], v[162:165]
	v_mfma_f32_16x16x32_f16 v[174:177], v[234:237], v[210:213], v[174:177]
	v_mfma_f32_16x16x32_f16 v[178:181], v[234:237], v[214:217], v[178:181]
	v_mfma_f32_16x16x32_f16 v[154:157], v[234:237], v[218:221], v[154:157]
	s_setprio 0
	ds_read_b128 v[8:11], v130 offset:12288
	ds_read_b128 v[68:71], v130 offset:14336
	v_cvt_pk_f16_f32 v63, v62, v63
	v_cvt_pk_f16_f32 v62, v60, v61
	ds_write_b64 v100, v[62:63] offset:61440
	s_add_u32 s80, s22, 0xe0b00
	s_addc_u32 s81, s90, 0
	s_add_u32 s100, s22, 0xc0b00
	s_addc_u32 s101, s90, 0
	global_load_dwordx4 v[56:59], v201, s[100:101] nt
	s_add_u32 s100, s22, 0xe0b00
	s_addc_u32 s101, s90, 0
	global_load_dwordx4 v[60:63], v201, s[100:101] nt
	s_setprio 1
	s_waitcnt lgkmcnt(1)
	v_mfma_f32_16x16x32_f16 v[88:91], v[8:11], v[210:213], v[88:91]
	v_mfma_f32_16x16x32_f16 v[234:237], v[8:11], v[206:209], v[72:75]
	v_mfma_f32_16x16x32_f16 v[158:161], v[8:11], v[214:217], v[158:161]
	v_mfma_f32_16x16x32_f16 v[166:169], v[8:11], v[218:221], v[166:169]
	v_mfma_f32_16x16x32_f16 v[182:185], v[68:71], v[206:209], v[182:185]
	v_mfma_f32_16x16x32_f16 v[190:193], v[68:71], v[210:213], v[190:193]
	v_mfma_f32_16x16x32_f16 v[202:205], v[68:71], v[214:217], v[202:205]
	v_mfma_f32_16x16x32_f16 v[186:189], v[68:71], v[218:221], v[186:189]
	s_setprio 0
	s_waitcnt vmcnt(6)
	s_waitcnt lgkmcnt(0)
	s_barrier
	ds_read_b128 v[206:209], v131 offset:32768
	ds_read_b128 v[210:213], v131 offset:34816
	ds_read_b128 v[214:217], v131 offset:36864
	ds_read_b128 v[218:221], v131 offset:38912
	ds_read_b128 v[68:71], v129 offset:32768
	ds_read_b128 v[72:75], v129 offset:34816
	s_add_u32 s80, s22, 0xc00
	v_lshl_add_u64 v[92:93], s[46:47], 0, v[196:197]
	s_addc_u32 s81, s90, 0
	v_readfirstlane_b32 s1, v94
	s_mov_b32 m0, s1
	v_cvt_pk_f16_f32 v3, v2, v3
	global_load_lds_dwordx4 v[92:93], off
	v_cvt_pk_f16_f32 v2, v0, v1
	ds_write_b64 v100, v[2:3]
	s_setprio 1
	s_waitcnt lgkmcnt(1)
	v_mfma_f32_16x16x32_f16 v[0:3], v[68:71], v[206:209], v[76:79]
	v_mfma_f32_16x16x32_f16 v[104:107], v[68:71], v[214:217], v[104:107]
	v_mfma_f32_16x16x32_f16 v[108:111], v[72:75], v[206:209], v[108:111]
	v_mfma_f32_16x16x32_f16 v[112:115], v[72:75], v[210:213], v[112:115]
	v_mfma_f32_16x16x32_f16 v[116:119], v[72:75], v[214:217], v[116:119]
	v_mfma_f32_16x16x32_f16 v[230:233], v[68:71], v[210:213], v[230:233]
	v_mfma_f32_16x16x32_f16 v[222:225], v[68:71], v[218:221], v[222:225]
	v_mfma_f32_16x16x32_f16 v[226:229], v[72:75], v[218:221], v[226:229]
	s_setprio 0
	ds_read_b128 v[72:75], v129 offset:36864
	ds_read_b128 v[76:79], v129 offset:38912
	v_readfirstlane_b32 s92, v99
	v_lshl_add_u64 v[68:69], v[92:93], 0, s[58:59]
	s_mov_b32 m0, s92
	v_cvt_pk_f16_f32 v15, v14, v15
	global_load_lds_dwordx4 v[68:69], off
	v_cvt_pk_f16_f32 v14, v12, v13
	ds_write_b64 v100, v[14:15] offset:4096
	s_add_u32 s80, s22, 0x20c00
	s_addc_u32 s81, s90, 0
	s_add_u32 s100, s22, 0xc00
	s_addc_u32 s101, s90, 0
	global_load_dwordx4 v[8:11], v201, s[100:101] nt
	s_setprio 1
	s_waitcnt lgkmcnt(1)
	v_mfma_f32_16x16x32_f16 v[12:15], v[72:75], v[206:209], v[242:245]
	v_mfma_f32_16x16x32_f16 v[120:123], v[72:75], v[218:221], v[120:123]
	v_mfma_f32_16x16x32_f16 v[124:127], v[76:79], v[206:209], v[124:127]
	v_mfma_f32_16x16x32_f16 v[146:149], v[76:79], v[214:217], v[146:149]
	v_mfma_f32_16x16x32_f16 v[134:137], v[76:79], v[218:221], v[134:137]
	v_mfma_f32_16x16x32_f16 v[242:245], v[72:75], v[210:213], v[80:83]
	v_mfma_f32_16x16x32_f16 v[138:141], v[72:75], v[214:217], v[138:141]
	v_mfma_f32_16x16x32_f16 v[142:145], v[76:79], v[210:213], v[142:145]
	s_setprio 0
	ds_read_b128 v[76:79], v129 offset:40960
	ds_read_b128 v[80:83], v129 offset:43008
	v_readfirstlane_b32 s91, v101
	v_lshl_add_u64 v[72:73], v[92:93], 0, s[60:61]
	s_mov_b32 m0, s91
	v_cvt_pk_f16_f32 v19, v18, v19
	global_load_lds_dwordx4 v[72:73], off
	v_cvt_pk_f16_f32 v18, v16, v17
	ds_write_b64 v100, v[18:19] offset:8192
	s_add_u32 s80, s22, 0x40c00
	s_addc_u32 s81, s90, 0
	s_add_u32 s100, s22, 0x20c00
	s_addc_u32 s101, s90, 0
	global_load_dwordx4 v[68:71], v201, s[100:101] nt
	s_setprio 1
	s_waitcnt lgkmcnt(1)
	v_mfma_f32_16x16x32_f16 v[16:19], v[76:79], v[206:209], v[238:241]
	v_mfma_f32_16x16x32_f16 v[238:241], v[76:79], v[210:213], v[84:87]
	v_mfma_f32_16x16x32_f16 v[170:173], v[76:79], v[214:217], v[170:173]
	v_mfma_f32_16x16x32_f16 v[150:153], v[76:79], v[218:221], v[150:153]
	v_mfma_f32_16x16x32_f16 v[162:165], v[80:83], v[206:209], v[162:165]
	v_mfma_f32_16x16x32_f16 v[174:177], v[80:83], v[210:213], v[174:177]
	v_mfma_f32_16x16x32_f16 v[178:181], v[80:83], v[214:217], v[178:181]
	v_mfma_f32_16x16x32_f16 v[154:157], v[80:83], v[218:221], v[154:157]
	s_setprio 0
	ds_read_b128 v[80:83], v129 offset:45056
	ds_read_b128 v[84:87], v129 offset:47104
	v_readfirstlane_b32 s73, v102
	v_lshl_add_u64 v[76:77], v[92:93], 0, s[62:63]
	s_mov_b32 m0, s73
	v_cvt_pk_f16_f32 v23, v22, v23
	global_load_lds_dwordx4 v[76:77], off
	v_cvt_pk_f16_f32 v22, v20, v21
	ds_write_b64 v100, v[22:23] offset:12288
	s_add_u32 s80, s22, 0x60c00
	s_addc_u32 s81, s90, 0
	s_add_u32 s100, s22, 0x40c00
	s_addc_u32 s101, s90, 0
	global_load_dwordx4 v[72:75], v201, s[100:101] nt
	s_setprio 1
	s_waitcnt lgkmcnt(1)
	v_mfma_f32_16x16x32_f16 v[20:23], v[80:83], v[206:209], v[234:237]
	v_mfma_f32_16x16x32_f16 v[234:237], v[80:83], v[210:213], v[88:91]
	v_mfma_f32_16x16x32_f16 v[158:161], v[80:83], v[214:217], v[158:161]
	v_mfma_f32_16x16x32_f16 v[166:169], v[80:83], v[218:221], v[166:169]
	v_mfma_f32_16x16x32_f16 v[182:185], v[84:87], v[206:209], v[182:185]
	v_mfma_f32_16x16x32_f16 v[190:193], v[84:87], v[210:213], v[190:193]
	v_mfma_f32_16x16x32_f16 v[202:205], v[84:87], v[214:217], v[202:205]
	v_mfma_f32_16x16x32_f16 v[186:189], v[84:87], v[218:221], v[186:189]
	s_setprio 0
	ds_read_b128 v[206:209], v128 offset:32768
	ds_read_b128 v[210:213], v128 offset:34816
	ds_read_b128 v[214:217], v128 offset:36864
	ds_read_b128 v[218:221], v128 offset:38912
	ds_read_b128 v[84:87], v130 offset:32768
	ds_read_b128 v[88:91], v130 offset:34816
	v_cvt_pk_f16_f32 v27, v26, v27
	v_cvt_pk_f16_f32 v26, v24, v25
	ds_write_b64 v100, v[26:27] offset:16384
	s_add_u32 s80, s22, 0x80c00
	s_addc_u32 s81, s90, 0
	s_add_u32 s100, s22, 0x60c00
	s_addc_u32 s101, s90, 0
	global_load_dwordx4 v[76:79], v201, s[100:101] nt
	s_setprio 1
	s_waitcnt lgkmcnt(1)
	v_mfma_f32_16x16x32_f16 v[24:27], v[84:87], v[206:209], v[0:3]
	v_mfma_f32_16x16x32_f16 v[104:107], v[84:87], v[214:217], v[104:107]
	v_mfma_f32_16x16x32_f16 v[108:111], v[88:91], v[206:209], v[108:111]
	v_mfma_f32_16x16x32_f16 v[112:115], v[88:91], v[210:213], v[112:115]
	v_mfma_f32_16x16x32_f16 v[116:119], v[88:91], v[214:217], v[116:119]
	v_mfma_f32_16x16x32_f16 v[230:233], v[84:87], v[210:213], v[230:233]
	v_mfma_f32_16x16x32_f16 v[222:225], v[84:87], v[218:221], v[222:225]
	v_mfma_f32_16x16x32_f16 v[226:229], v[88:91], v[218:221], v[226:229]
	s_setprio 0
	ds_read_b128 v[0:3], v130 offset:36864
	ds_read_b128 v[88:91], v130 offset:38912
	v_cvt_pk_f16_f32 v31, v30, v31
	v_cvt_pk_f16_f32 v30, v28, v29
	ds_write_b64 v100, v[30:31] offset:20480
	s_add_u32 s80, s22, 0xa0c00
	s_addc_u32 s81, s90, 0
	s_add_u32 s100, s22, 0x80c00
	s_addc_u32 s101, s90, 0
	global_load_dwordx4 v[80:83], v201, s[100:101] nt
	s_setprio 1
	s_waitcnt lgkmcnt(1)
	v_mfma_f32_16x16x32_f16 v[12:15], v[0:3], v[206:209], v[12:15]
	v_mfma_f32_16x16x32_f16 v[28:31], v[0:3], v[210:213], v[242:245]
	v_mfma_f32_16x16x32_f16 v[120:123], v[0:3], v[218:221], v[120:123]
	v_mfma_f32_16x16x32_f16 v[124:127], v[88:91], v[206:209], v[124:127]
	v_mfma_f32_16x16x32_f16 v[146:149], v[88:91], v[214:217], v[146:149]
	v_mfma_f32_16x16x32_f16 v[134:137], v[88:91], v[218:221], v[134:137]
	v_mfma_f32_16x16x32_f16 v[138:141], v[0:3], v[214:217], v[138:141]
	v_mfma_f32_16x16x32_f16 v[142:145], v[88:91], v[210:213], v[142:145]
	s_setprio 0
	ds_read_b128 v[0:3], v130 offset:40960
	ds_read_b128 v[242:245], v130 offset:43008
	v_cvt_pk_f16_f32 v35, v34, v35
	v_cvt_pk_f16_f32 v34, v32, v33
	ds_write_b64 v100, v[34:35] offset:24576
	s_add_u32 s80, s22, 0xc0c00
	s_addc_u32 s81, s90, 0
	s_add_u32 s100, s22, 0xa0c00
	s_addc_u32 s101, s90, 0
	global_load_dwordx4 v[84:87], v201, s[100:101] nt
	s_setprio 1
	s_waitcnt lgkmcnt(1)
	v_mfma_f32_16x16x32_f16 v[16:19], v[0:3], v[206:209], v[16:19]
	v_mfma_f32_16x16x32_f16 v[32:35], v[0:3], v[210:213], v[238:241]
	v_mfma_f32_16x16x32_f16 v[170:173], v[0:3], v[214:217], v[170:173]
	v_mfma_f32_16x16x32_f16 v[150:153], v[0:3], v[218:221], v[150:153]
	v_mfma_f32_16x16x32_f16 v[162:165], v[242:245], v[206:209], v[162:165]
	v_mfma_f32_16x16x32_f16 v[174:177], v[242:245], v[210:213], v[174:177]
	v_mfma_f32_16x16x32_f16 v[178:181], v[242:245], v[214:217], v[178:181]
	v_mfma_f32_16x16x32_f16 v[154:157], v[242:245], v[218:221], v[154:157]
	s_setprio 0
	ds_read_b128 v[0:3], v130 offset:45056
	ds_read_b128 v[238:241], v130 offset:47104
	v_cvt_pk_f16_f32 v39, v38, v39
	v_cvt_pk_f16_f32 v38, v36, v37
	ds_write_b64 v100, v[38:39] offset:28672
	s_add_u32 s80, s22, 0xe0c00
	s_addc_u32 s81, s90, 0
	s_add_u32 s100, s22, 0xc0c00
	s_addc_u32 s101, s90, 0
	global_load_dwordx4 v[88:91], v201, s[100:101] nt
	s_add_u32 s100, s22, 0xe0c00
	s_addc_u32 s101, s90, 0
	global_load_dwordx4 v[36:39], v201, s[100:101] nt
	s_setprio 1
	s_waitcnt lgkmcnt(1)
	v_mfma_f32_16x16x32_f16 v[20:23], v[0:3], v[206:209], v[20:23]
	v_mfma_f32_16x16x32_f16 v[234:237], v[0:3], v[210:213], v[234:237]
	v_mfma_f32_16x16x32_f16 v[158:161], v[0:3], v[214:217], v[158:161]
	v_mfma_f32_16x16x32_f16 v[166:169], v[0:3], v[218:221], v[166:169]
	v_mfma_f32_16x16x32_f16 v[182:185], v[238:241], v[206:209], v[182:185]
	v_mfma_f32_16x16x32_f16 v[190:193], v[238:241], v[210:213], v[190:193]
	v_mfma_f32_16x16x32_f16 v[202:205], v[238:241], v[214:217], v[202:205]
	v_mfma_f32_16x16x32_f16 v[186:189], v[238:241], v[218:221], v[186:189]
	s_setprio 0
	s_waitcnt vmcnt(6)
	s_waitcnt lgkmcnt(0)
	s_barrier
	ds_read_b128 v[206:209], v131
	ds_read_b128 v[210:213], v131 offset:2048
	ds_read_b128 v[214:217], v131 offset:4096
	ds_read_b128 v[218:221], v131 offset:6144
	ds_read_b128 v[238:241], v129
	ds_read_b128 v[242:245], v129 offset:2048
	s_add_u32 s80, s22, 0xd00
	v_lshl_add_u64 v[92:93], s[48:49], 0, v[196:197]
	s_addc_u32 s81, s90, 0
	s_mov_b32 m0, s0
	v_cvt_pk_f16_f32 v1, v6, v7
	global_load_lds_dwordx4 v[92:93], off
	v_cvt_pk_f16_f32 v0, v4, v5
	ds_write_b64 v100, v[0:1] offset:32768
	s_setprio 1
	s_waitcnt lgkmcnt(1)
	v_mfma_f32_16x16x32_f16 v[24:27], v[238:241], v[206:209], v[24:27]
	v_mfma_f32_16x16x32_f16 v[104:107], v[238:241], v[214:217], v[104:107]
	v_mfma_f32_16x16x32_f16 v[108:111], v[242:245], v[206:209], v[108:111]
	v_mfma_f32_16x16x32_f16 v[112:115], v[242:245], v[210:213], v[112:115]
	v_mfma_f32_16x16x32_f16 v[116:119], v[242:245], v[214:217], v[116:119]
	v_mfma_f32_16x16x32_f16 v[230:233], v[238:241], v[210:213], v[230:233]
	v_mfma_f32_16x16x32_f16 v[222:225], v[238:241], v[218:221], v[222:225]
	v_mfma_f32_16x16x32_f16 v[226:229], v[242:245], v[218:221], v[226:229]
	s_setprio 0
	ds_read_b128 v[238:241], v129 offset:4096
	ds_read_b128 v[242:245], v129 offset:6144
	s_mov_b32 m0, s72
	v_lshl_add_u64 v[4:5], v[92:93], 0, s[58:59]
	global_load_lds_dwordx4 v[4:5], off
	v_cvt_pk_f16_f32 v5, v66, v67
	v_cvt_pk_f16_f32 v4, v64, v65
	ds_write_b64 v100, v[4:5] offset:36864
	s_add_u32 s80, s22, 0x20d00
	s_addc_u32 s81, s90, 0
	s_add_u32 s100, s22, 0xd00
	s_addc_u32 s101, s90, 0
	global_load_dwordx4 v[0:3], v201, s[100:101] nt
	s_setprio 1
	s_waitcnt lgkmcnt(1)
	v_mfma_f32_16x16x32_f16 v[64:67], v[238:241], v[206:209], v[12:15]
	v_mfma_f32_16x16x32_f16 v[28:31], v[238:241], v[210:213], v[28:31]
	v_mfma_f32_16x16x32_f16 v[120:123], v[238:241], v[218:221], v[120:123]
	v_mfma_f32_16x16x32_f16 v[124:127], v[242:245], v[206:209], v[124:127]
	v_mfma_f32_16x16x32_f16 v[146:149], v[242:245], v[214:217], v[146:149]
	v_mfma_f32_16x16x32_f16 v[134:137], v[242:245], v[218:221], v[134:137]
	v_mfma_f32_16x16x32_f16 v[138:141], v[238:241], v[214:217], v[138:141]
	v_mfma_f32_16x16x32_f16 v[142:145], v[242:245], v[210:213], v[142:145]
	s_setprio 0
	ds_read_b128 v[238:241], v129 offset:8192
	ds_read_b128 v[242:245], v129 offset:10240
	s_mov_b32 m0, s71
	v_lshl_add_u64 v[12:13], v[92:93], 0, s[60:61]
	global_load_lds_dwordx4 v[12:13], off
	v_cvt_pk_f16_f32 v13, v42, v43
	v_cvt_pk_f16_f32 v12, v40, v41
	ds_write_b64 v100, v[12:13] offset:40960
	s_add_u32 s80, s22, 0x40d00
	s_addc_u32 s81, s90, 0
	s_add_u32 s100, s22, 0x20d00
	s_addc_u32 s101, s90, 0
	global_load_dwordx4 v[4:7], v201, s[100:101] nt
	s_setprio 1
	s_waitcnt lgkmcnt(1)
	v_mfma_f32_16x16x32_f16 v[40:43], v[238:241], v[206:209], v[16:19]
	v_mfma_f32_16x16x32_f16 v[32:35], v[238:241], v[210:213], v[32:35]
	v_mfma_f32_16x16x32_f16 v[170:173], v[238:241], v[214:217], v[170:173]
	v_mfma_f32_16x16x32_f16 v[150:153], v[238:241], v[218:221], v[150:153]
	v_mfma_f32_16x16x32_f16 v[162:165], v[242:245], v[206:209], v[162:165]
	v_mfma_f32_16x16x32_f16 v[174:177], v[242:245], v[210:213], v[174:177]
	v_mfma_f32_16x16x32_f16 v[178:181], v[242:245], v[214:217], v[178:181]
	v_mfma_f32_16x16x32_f16 v[154:157], v[242:245], v[218:221], v[154:157]
	s_setprio 0
	ds_read_b128 v[238:241], v129 offset:12288
	ds_read_b128 v[242:245], v129 offset:14336
	s_mov_b32 m0, s70
	v_lshl_add_u64 v[16:17], v[92:93], 0, s[62:63]
	global_load_lds_dwordx4 v[16:17], off
	v_cvt_pk_f16_f32 v17, v46, v47
	v_cvt_pk_f16_f32 v16, v44, v45
	ds_write_b64 v100, v[16:17] offset:45056
	s_add_u32 s70, s22, 0x60d00
	s_addc_u32 s71, s90, 0
	s_add_u32 s100, s22, 0x40d00
	s_addc_u32 s101, s90, 0
	global_load_dwordx4 v[12:15], v201, s[100:101] nt
	s_setprio 1
	s_waitcnt lgkmcnt(1)
	v_mfma_f32_16x16x32_f16 v[44:47], v[238:241], v[206:209], v[20:23]
	v_mfma_f32_16x16x32_f16 v[234:237], v[238:241], v[210:213], v[234:237]
	v_mfma_f32_16x16x32_f16 v[158:161], v[238:241], v[214:217], v[158:161]
	v_mfma_f32_16x16x32_f16 v[166:169], v[238:241], v[218:221], v[166:169]
	v_mfma_f32_16x16x32_f16 v[182:185], v[242:245], v[206:209], v[182:185]
	v_mfma_f32_16x16x32_f16 v[190:193], v[242:245], v[210:213], v[190:193]
	v_mfma_f32_16x16x32_f16 v[202:205], v[242:245], v[214:217], v[202:205]
	v_mfma_f32_16x16x32_f16 v[186:189], v[242:245], v[218:221], v[186:189]
	s_setprio 0
	ds_read_b128 v[206:209], v128
	ds_read_b128 v[210:213], v128 offset:2048
	ds_read_b128 v[214:217], v128 offset:4096
	ds_read_b128 v[218:221], v128 offset:6144
	ds_read_b128 v[238:241], v130
	ds_read_b128 v[242:245], v130 offset:2048
	v_cvt_pk_f16_f32 v21, v50, v51
	v_cvt_pk_f16_f32 v20, v48, v49
	ds_write_b64 v100, v[20:21] offset:49152
	s_add_u32 s70, s22, 0x80d00
	s_addc_u32 s71, s90, 0
	s_add_u32 s100, s22, 0x60d00
	s_addc_u32 s101, s90, 0
	global_load_dwordx4 v[16:19], v201, s[100:101] nt
	s_setprio 1
	s_waitcnt lgkmcnt(1)
	v_mfma_f32_16x16x32_f16 v[48:51], v[238:241], v[206:209], v[24:27]
	v_mfma_f32_16x16x32_f16 v[104:107], v[238:241], v[214:217], v[104:107]
	v_mfma_f32_16x16x32_f16 v[108:111], v[242:245], v[206:209], v[108:111]
	v_mfma_f32_16x16x32_f16 v[112:115], v[242:245], v[210:213], v[112:115]
	v_mfma_f32_16x16x32_f16 v[116:119], v[242:245], v[214:217], v[116:119]
	v_mfma_f32_16x16x32_f16 v[230:233], v[238:241], v[210:213], v[230:233]
	v_mfma_f32_16x16x32_f16 v[222:225], v[238:241], v[218:221], v[222:225]
	v_mfma_f32_16x16x32_f16 v[226:229], v[242:245], v[218:221], v[226:229]
	s_setprio 0
	ds_read_b128 v[238:241], v130 offset:4096
	ds_read_b128 v[242:245], v130 offset:6144
	v_cvt_pk_f16_f32 v25, v54, v55
	v_cvt_pk_f16_f32 v24, v52, v53
	ds_write_b64 v100, v[24:25] offset:53248
	s_add_u32 s70, s22, 0xa0d00
	s_addc_u32 s71, s90, 0
	s_add_u32 s100, s22, 0x80d00
	s_addc_u32 s101, s90, 0
	global_load_dwordx4 v[20:23], v201, s[100:101] nt
	s_setprio 1
	s_waitcnt lgkmcnt(1)
	v_mfma_f32_16x16x32_f16 v[52:55], v[238:241], v[206:209], v[64:67]
	v_mfma_f32_16x16x32_f16 v[64:67], v[238:241], v[210:213], v[28:31]
	v_mfma_f32_16x16x32_f16 v[120:123], v[238:241], v[218:221], v[120:123]
	v_mfma_f32_16x16x32_f16 v[124:127], v[242:245], v[206:209], v[124:127]
	v_mfma_f32_16x16x32_f16 v[146:149], v[242:245], v[214:217], v[146:149]
	v_mfma_f32_16x16x32_f16 v[134:137], v[242:245], v[218:221], v[134:137]
	v_mfma_f32_16x16x32_f16 v[138:141], v[238:241], v[214:217], v[138:141]
	v_mfma_f32_16x16x32_f16 v[142:145], v[242:245], v[210:213], v[142:145]
	s_setprio 0
	ds_read_b128 v[238:241], v130 offset:8192
	ds_read_b128 v[242:245], v130 offset:10240
	v_cvt_pk_f16_f32 v29, v58, v59
	v_cvt_pk_f16_f32 v28, v56, v57
	ds_write_b64 v100, v[28:29] offset:57344
	s_add_u32 s70, s22, 0xc0d00
	s_addc_u32 s71, s90, 0
	s_add_u32 s100, s22, 0xa0d00
	s_addc_u32 s101, s90, 0
	global_load_dwordx4 v[24:27], v201, s[100:101] nt
	s_setprio 1
	s_waitcnt lgkmcnt(1)
	v_mfma_f32_16x16x32_f16 v[56:59], v[238:241], v[206:209], v[40:43]
	v_mfma_f32_16x16x32_f16 v[246:249], v[238:241], v[210:213], v[32:35]
	v_mfma_f32_16x16x32_f16 v[170:173], v[238:241], v[214:217], v[170:173]
	v_mfma_f32_16x16x32_f16 v[150:153], v[238:241], v[218:221], v[150:153]
	v_mfma_f32_16x16x32_f16 v[162:165], v[242:245], v[206:209], v[162:165]
	v_mfma_f32_16x16x32_f16 v[174:177], v[242:245], v[210:213], v[174:177]
	v_mfma_f32_16x16x32_f16 v[178:181], v[242:245], v[214:217], v[178:181]
	v_mfma_f32_16x16x32_f16 v[154:157], v[242:245], v[218:221], v[154:157]
	s_setprio 0
	ds_read_b128 v[40:43], v130 offset:12288
	ds_read_b128 v[238:241], v130 offset:14336
	v_cvt_pk_f16_f32 v33, v62, v63
	v_cvt_pk_f16_f32 v32, v60, v61
	ds_write_b64 v100, v[32:33] offset:61440
	s_add_u32 s70, s22, 0xe0d00
	s_addc_u32 s71, s90, 0
	s_add_u32 s100, s22, 0xc0d00
	s_addc_u32 s101, s90, 0
	global_load_dwordx4 v[28:31], v201, s[100:101] nt
	s_add_u32 s100, s22, 0xe0d00
	s_addc_u32 s101, s90, 0
	global_load_dwordx4 v[32:35], v201, s[100:101] nt
	s_setprio 1
	s_waitcnt lgkmcnt(1)
	v_mfma_f32_16x16x32_f16 v[60:63], v[40:43], v[206:209], v[44:47]
	v_mfma_f32_16x16x32_f16 v[234:237], v[40:43], v[210:213], v[234:237]
	v_mfma_f32_16x16x32_f16 v[158:161], v[40:43], v[214:217], v[158:161]
	v_mfma_f32_16x16x32_f16 v[166:169], v[40:43], v[218:221], v[166:169]
	v_mfma_f32_16x16x32_f16 v[182:185], v[238:241], v[206:209], v[182:185]
	v_mfma_f32_16x16x32_f16 v[190:193], v[238:241], v[210:213], v[190:193]
	v_mfma_f32_16x16x32_f16 v[202:205], v[238:241], v[214:217], v[202:205]
	v_mfma_f32_16x16x32_f16 v[186:189], v[238:241], v[218:221], v[186:189]
	s_setprio 0
	s_waitcnt vmcnt(6)
	s_waitcnt lgkmcnt(0)
	s_barrier
	ds_read_b128 v[206:209], v131 offset:32768
	ds_read_b128 v[210:213], v131 offset:34816
	ds_read_b128 v[214:217], v131 offset:36864
	ds_read_b128 v[218:221], v131 offset:38912
	ds_read_b128 v[40:43], v129 offset:32768
	ds_read_b128 v[44:47], v129 offset:34816
	s_add_u32 s70, s22, 0xe00
	v_lshl_add_u64 v[92:93], s[50:51], 0, v[196:197]
	s_addc_u32 s71, s90, 0
	s_mov_b32 m0, s1
	v_cvt_pk_f16_f32 v11, v10, v11
	global_load_lds_dwordx4 v[92:93], off
	v_cvt_pk_f16_f32 v10, v8, v9
	ds_write_b64 v100, v[10:11]
	s_setprio 1
	s_waitcnt lgkmcnt(1)
	v_mfma_f32_16x16x32_f16 v[104:107], v[40:43], v[214:217], v[104:107]
	v_mfma_f32_16x16x32_f16 v[108:111], v[44:47], v[206:209], v[108:111]
	v_mfma_f32_16x16x32_f16 v[112:115], v[44:47], v[210:213], v[112:115]
	v_mfma_f32_16x16x32_f16 v[116:119], v[44:47], v[214:217], v[116:119]
	v_mfma_f32_16x16x32_f16 v[238:241], v[40:43], v[206:209], v[48:51]
	v_mfma_f32_16x16x32_f16 v[230:233], v[40:43], v[210:213], v[230:233]
	v_mfma_f32_16x16x32_f16 v[222:225], v[40:43], v[218:221], v[222:225]
	v_mfma_f32_16x16x32_f16 v[226:229], v[44:47], v[218:221], v[226:229]
	s_setprio 0
	ds_read_b128 v[44:47], v129 offset:36864
	ds_read_b128 v[48:51], v129 offset:38912
	s_mov_b32 m0, s92
	v_lshl_add_u64 v[40:41], v[92:93], 0, s[58:59]
	global_load_lds_dwordx4 v[40:41], off
	v_cvt_pk_f16_f32 v41, v70, v71
	v_cvt_pk_f16_f32 v40, v68, v69
	ds_write_b64 v100, v[40:41] offset:4096
	s_add_u32 s0, s22, 0x20e00
	s_addc_u32 s1, s90, 0
	s_add_u32 s100, s22, 0xe00
	s_addc_u32 s101, s90, 0
	global_load_dwordx4 v[8:11], v201, s[100:101] nt
	s_setprio 1
	s_waitcnt lgkmcnt(1)
	v_mfma_f32_16x16x32_f16 v[68:71], v[44:47], v[206:209], v[52:55]
	v_mfma_f32_16x16x32_f16 v[64:67], v[44:47], v[210:213], v[64:67]
	v_mfma_f32_16x16x32_f16 v[120:123], v[44:47], v[218:221], v[120:123]
	v_mfma_f32_16x16x32_f16 v[124:127], v[48:51], v[206:209], v[124:127]
	v_mfma_f32_16x16x32_f16 v[146:149], v[48:51], v[214:217], v[146:149]
	v_mfma_f32_16x16x32_f16 v[134:137], v[48:51], v[218:221], v[134:137]
	v_mfma_f32_16x16x32_f16 v[138:141], v[44:47], v[214:217], v[138:141]
	v_mfma_f32_16x16x32_f16 v[142:145], v[48:51], v[210:213], v[142:145]
	s_setprio 0
	ds_read_b128 v[48:51], v129 offset:40960
	ds_read_b128 v[52:55], v129 offset:43008
	s_mov_b32 m0, s91
	v_lshl_add_u64 v[44:45], v[92:93], 0, s[60:61]
	global_load_lds_dwordx4 v[44:45], off
	v_cvt_pk_f16_f32 v45, v74, v75
	v_cvt_pk_f16_f32 v44, v72, v73
	ds_write_b64 v100, v[44:45] offset:8192
	s_add_u32 s0, s22, 0x40e00
	s_addc_u32 s1, s90, 0
	s_add_u32 s100, s22, 0x20e00
	s_addc_u32 s101, s90, 0
	global_load_dwordx4 v[40:43], v201, s[100:101] nt
	s_setprio 1
	s_waitcnt lgkmcnt(1)
	v_mfma_f32_16x16x32_f16 v[72:75], v[48:51], v[206:209], v[56:59]
	v_mfma_f32_16x16x32_f16 v[242:245], v[48:51], v[210:213], v[246:249]
	v_mfma_f32_16x16x32_f16 v[170:173], v[48:51], v[214:217], v[170:173]
	v_mfma_f32_16x16x32_f16 v[150:153], v[48:51], v[218:221], v[150:153]
	v_mfma_f32_16x16x32_f16 v[162:165], v[52:55], v[206:209], v[162:165]
	v_mfma_f32_16x16x32_f16 v[174:177], v[52:55], v[210:213], v[174:177]
	v_mfma_f32_16x16x32_f16 v[178:181], v[52:55], v[214:217], v[178:181]
	v_mfma_f32_16x16x32_f16 v[154:157], v[52:55], v[218:221], v[154:157]
	s_setprio 0
	ds_read_b128 v[52:55], v129 offset:45056
	ds_read_b128 v[56:59], v129 offset:47104
	s_mov_b32 m0, s73
	v_lshl_add_u64 v[48:49], v[92:93], 0, s[62:63]
	global_load_lds_dwordx4 v[48:49], off
	v_cvt_pk_f16_f32 v49, v78, v79
	v_cvt_pk_f16_f32 v48, v76, v77
	ds_write_b64 v100, v[48:49] offset:12288
	s_add_u32 s0, s22, 0x60e00
	s_addc_u32 s1, s90, 0
	s_add_u32 s100, s22, 0x40e00
	s_addc_u32 s101, s90, 0
	global_load_dwordx4 v[44:47], v201, s[100:101] nt
	s_setprio 1
	s_waitcnt lgkmcnt(1)
	v_mfma_f32_16x16x32_f16 v[76:79], v[52:55], v[206:209], v[60:63]
	v_mfma_f32_16x16x32_f16 v[234:237], v[52:55], v[210:213], v[234:237]
	v_mfma_f32_16x16x32_f16 v[158:161], v[52:55], v[214:217], v[158:161]
	v_mfma_f32_16x16x32_f16 v[166:169], v[52:55], v[218:221], v[166:169]
	v_mfma_f32_16x16x32_f16 v[182:185], v[56:59], v[206:209], v[182:185]
	v_mfma_f32_16x16x32_f16 v[190:193], v[56:59], v[210:213], v[190:193]
	v_mfma_f32_16x16x32_f16 v[202:205], v[56:59], v[214:217], v[202:205]
	v_mfma_f32_16x16x32_f16 v[186:189], v[56:59], v[218:221], v[186:189]
	s_setprio 0
	ds_read_b128 v[206:209], v128 offset:32768
	ds_read_b128 v[210:213], v128 offset:34816
	ds_read_b128 v[214:217], v128 offset:36864
	ds_read_b128 v[218:221], v128 offset:38912
	ds_read_b128 v[56:59], v130 offset:32768
	ds_read_b128 v[60:63], v130 offset:34816
	v_cvt_pk_f16_f32 v53, v82, v83
	v_cvt_pk_f16_f32 v52, v80, v81
	ds_write_b64 v100, v[52:53] offset:16384
	s_add_u32 s0, s22, 0x80e00
	s_addc_u32 s1, s90, 0
	s_add_u32 s100, s22, 0x60e00
	s_addc_u32 s101, s90, 0
	global_load_dwordx4 v[48:51], v201, s[100:101] nt
	s_setprio 1
	s_waitcnt lgkmcnt(1)
	v_mfma_f32_16x16x32_f16 v[80:83], v[56:59], v[206:209], v[238:241]
	v_mfma_f32_16x16x32_f16 v[104:107], v[56:59], v[214:217], v[104:107]
	v_mfma_f32_16x16x32_f16 v[108:111], v[60:63], v[206:209], v[108:111]
	v_mfma_f32_16x16x32_f16 v[112:115], v[60:63], v[210:213], v[112:115]
	v_mfma_f32_16x16x32_f16 v[116:119], v[60:63], v[214:217], v[116:119]
	v_mfma_f32_16x16x32_f16 v[230:233], v[56:59], v[210:213], v[230:233]
	v_mfma_f32_16x16x32_f16 v[222:225], v[56:59], v[218:221], v[222:225]
	v_mfma_f32_16x16x32_f16 v[226:229], v[60:63], v[218:221], v[226:229]
	s_setprio 0
	ds_read_b128 v[60:63], v130 offset:36864
	ds_read_b128 v[238:241], v130 offset:38912
	v_cvt_pk_f16_f32 v57, v86, v87
	v_cvt_pk_f16_f32 v56, v84, v85
	ds_write_b64 v100, v[56:57] offset:20480
	s_add_u32 s0, s22, 0xa0e00
	s_addc_u32 s1, s90, 0
	s_add_u32 s100, s22, 0x80e00
	s_addc_u32 s101, s90, 0
	global_load_dwordx4 v[52:55], v201, s[100:101] nt
	s_setprio 1
	s_waitcnt lgkmcnt(1)
	v_mfma_f32_16x16x32_f16 v[68:71], v[60:63], v[206:209], v[68:71]
	v_mfma_f32_16x16x32_f16 v[64:67], v[60:63], v[210:213], v[64:67]
	v_mfma_f32_16x16x32_f16 v[84:87], v[60:63], v[214:217], v[138:141]
	v_mfma_f32_16x16x32_f16 v[120:123], v[60:63], v[218:221], v[120:123]
	v_mfma_f32_16x16x32_f16 v[124:127], v[238:241], v[206:209], v[124:127]
	v_mfma_f32_16x16x32_f16 v[134:137], v[238:241], v[218:221], v[134:137]
	v_mfma_f32_16x16x32_f16 v[138:141], v[238:241], v[210:213], v[142:145]
	v_mfma_f32_16x16x32_f16 v[142:145], v[238:241], v[214:217], v[146:149]
	s_setprio 0
	s_nop 1
	ds_read_b128 v[146:149], v130 offset:40960
	ds_read_b128 v[238:241], v130 offset:43008
	v_cvt_pk_f16_f32 v61, v90, v91
	v_cvt_pk_f16_f32 v60, v88, v89
	ds_write_b64 v100, v[60:61] offset:24576
	s_add_u32 s0, s22, 0xc0e00
	s_addc_u32 s1, s90, 0
	s_add_u32 s100, s22, 0xa0e00
	s_addc_u32 s101, s90, 0
	global_load_dwordx4 v[56:59], v201, s[100:101] nt
	s_setprio 1
	s_waitcnt lgkmcnt(1)
	v_mfma_f32_16x16x32_f16 v[72:75], v[146:149], v[206:209], v[72:75]
	v_mfma_f32_16x16x32_f16 v[88:91], v[146:149], v[210:213], v[242:245]
	v_mfma_f32_16x16x32_f16 v[170:173], v[146:149], v[214:217], v[170:173]
	v_mfma_f32_16x16x32_f16 v[146:149], v[146:149], v[218:221], v[150:153]
	v_mfma_f32_16x16x32_f16 v[150:153], v[238:241], v[206:209], v[162:165]
	v_mfma_f32_16x16x32_f16 v[162:165], v[238:241], v[210:213], v[174:177]
	v_mfma_f32_16x16x32_f16 v[174:177], v[238:241], v[214:217], v[178:181]
	v_mfma_f32_16x16x32_f16 v[154:157], v[238:241], v[218:221], v[154:157]
	s_setprio 0
	s_nop 0
	ds_read_b128 v[178:181], v130 offset:45056
	ds_read_b128 v[238:241], v130 offset:47104
	v_cvt_pk_f16_f32 v39, v38, v39
	v_cvt_pk_f16_f32 v38, v36, v37
	ds_write_b64 v100, v[38:39] offset:28672
	s_add_u32 s0, s22, 0xe0e00
	s_addc_u32 s1, s90, 0
	s_add_u32 s100, s22, 0xc0e00
	s_addc_u32 s101, s90, 0
	global_load_dwordx4 v[60:63], v201, s[100:101] nt
	s_add_u32 s100, s22, 0xe0e00
	s_addc_u32 s101, s90, 0
	global_load_dwordx4 v[36:39], v201, s[100:101] nt
	s_setprio 1
	s_waitcnt lgkmcnt(1)
	v_mfma_f32_16x16x32_f16 v[76:79], v[178:181], v[206:209], v[76:79]
	v_mfma_f32_16x16x32_f16 v[234:237], v[178:181], v[210:213], v[234:237]
	v_mfma_f32_16x16x32_f16 v[158:161], v[178:181], v[214:217], v[158:161]
	v_mfma_f32_16x16x32_f16 v[166:169], v[178:181], v[218:221], v[166:169]
	v_mfma_f32_16x16x32_f16 v[178:181], v[238:241], v[206:209], v[182:185]
	v_mfma_f32_16x16x32_f16 v[182:185], v[238:241], v[210:213], v[190:193]
	v_mfma_f32_16x16x32_f16 v[190:193], v[238:241], v[214:217], v[202:205]
	v_mfma_f32_16x16x32_f16 v[186:189], v[238:241], v[218:221], v[186:189]
	s_setprio 0
	s_waitcnt vmcnt(6)
	s_waitcnt lgkmcnt(0)
	s_barrier
	ds_read_b128 v[202:205], v131
	ds_read_b128 v[206:209], v131 offset:2048
	ds_read_b128 v[210:213], v131 offset:4096
	ds_read_b128 v[214:217], v131 offset:6144
	ds_read_b128 v[218:221], v129
	ds_read_b128 v[238:241], v129 offset:2048
	s_add_u32 s70, s22, 0xf00
	v_lshl_add_u64 v[92:93], s[52:53], 0, v[196:197]
	s_addc_u32 s71, s90, 0
	v_readfirstlane_b32 s0, v95
	s_mov_b32 m0, s0
	v_cvt_pk_f16_f32 v3, v2, v3
	global_load_lds_dwordx4 v[92:93], off
	v_cvt_pk_f16_f32 v2, v0, v1
	ds_write_b64 v100, v[2:3] offset:32768
	s_setprio 1
	s_waitcnt lgkmcnt(1)
	v_mfma_f32_16x16x32_f16 v[80:83], v[218:221], v[202:205], v[80:83]
	v_mfma_f32_16x16x32_f16 v[104:107], v[218:221], v[210:213], v[104:107]
	v_mfma_f32_16x16x32_f16 v[108:111], v[238:241], v[202:205], v[108:111]
	v_mfma_f32_16x16x32_f16 v[112:115], v[238:241], v[206:209], v[112:115]
	v_mfma_f32_16x16x32_f16 v[116:119], v[238:241], v[210:213], v[116:119]
	v_mfma_f32_16x16x32_f16 v[230:233], v[218:221], v[206:209], v[230:233]
	v_mfma_f32_16x16x32_f16 v[218:221], v[218:221], v[214:217], v[222:225]
	v_mfma_f32_16x16x32_f16 v[222:225], v[238:241], v[214:217], v[226:229]
	s_setprio 0
	s_nop 1
	ds_read_b128 v[226:229], v129 offset:4096
	ds_read_b128 v[238:241], v129 offset:6144
	v_readfirstlane_b32 s1, v96
	v_lshl_add_u64 v[198:199], v[92:93], 0, s[58:59]
	s_mov_b32 m0, s1
	v_cvt_pk_f16_f32 v7, v6, v7
	global_load_lds_dwordx4 v[198:199], off
	v_cvt_pk_f16_f32 v6, v4, v5
	ds_write_b64 v100, v[6:7] offset:36864
	s_add_u32 s70, s22, 0x20f00
	s_addc_u32 s71, s90, 0
	s_add_u32 s100, s22, 0xf00
	s_addc_u32 s101, s90, 0
	global_load_dwordx4 v[0:3], v201, s[100:101] nt
	s_setprio 1
	s_waitcnt lgkmcnt(1)
	v_mfma_f32_16x16x32_f16 v[68:71], v[226:229], v[202:205], v[68:71]
	v_mfma_f32_16x16x32_f16 v[64:67], v[226:229], v[206:209], v[64:67]
	v_mfma_f32_16x16x32_f16 v[84:87], v[226:229], v[210:213], v[84:87]
	v_mfma_f32_16x16x32_f16 v[120:123], v[226:229], v[214:217], v[120:123]
	v_mfma_f32_16x16x32_f16 v[124:127], v[238:241], v[202:205], v[124:127]
	v_mfma_f32_16x16x32_f16 v[134:137], v[238:241], v[214:217], v[134:137]
	v_mfma_f32_16x16x32_f16 v[138:141], v[238:241], v[206:209], v[138:141]
	v_mfma_f32_16x16x32_f16 v[142:145], v[238:241], v[210:213], v[142:145]
	s_setprio 0
	ds_read_b128 v[226:229], v129 offset:8192
	ds_read_b128 v[238:241], v129 offset:10240
	v_readfirstlane_b32 s70, v97
	v_lshl_add_u64 v[198:199], v[92:93], 0, s[60:61]
	s_mov_b32 m0, s70
	v_cvt_pk_f16_f32 v15, v14, v15
	global_load_lds_dwordx4 v[198:199], off
	v_cvt_pk_f16_f32 v14, v12, v13
	ds_write_b64 v100, v[14:15] offset:40960
	s_add_u32 s72, s22, 0x40f00
	s_addc_u32 s73, s90, 0
	s_add_u32 s100, s22, 0x20f00
	s_addc_u32 s101, s90, 0
	global_load_dwordx4 v[4:7], v201, s[100:101] nt
	s_setprio 1
	s_waitcnt lgkmcnt(1)
	v_mfma_f32_16x16x32_f16 v[72:75], v[226:229], v[202:205], v[72:75]
	v_mfma_f32_16x16x32_f16 v[88:91], v[226:229], v[206:209], v[88:91]
	v_mfma_f32_16x16x32_f16 v[146:149], v[226:229], v[214:217], v[146:149]
	v_mfma_f32_16x16x32_f16 v[170:173], v[226:229], v[210:213], v[170:173]
	v_mfma_f32_16x16x32_f16 v[150:153], v[238:241], v[202:205], v[150:153]
	v_mfma_f32_16x16x32_f16 v[162:165], v[238:241], v[206:209], v[162:165]
	v_mfma_f32_16x16x32_f16 v[174:177], v[238:241], v[210:213], v[174:177]
	v_mfma_f32_16x16x32_f16 v[154:157], v[238:241], v[214:217], v[154:157]
	s_setprio 0
	ds_read_b128 v[226:229], v129 offset:12288
	ds_read_b128 v[238:241], v129 offset:14336
	v_readfirstlane_b32 s71, v98
	v_lshl_add_u64 v[92:93], v[92:93], 0, s[62:63]
	s_mov_b32 m0, s71
	v_cvt_pk_f16_f32 v19, v18, v19
	global_load_lds_dwordx4 v[92:93], off
	v_cvt_pk_f16_f32 v18, v16, v17
	ds_write_b64 v100, v[18:19] offset:45056
	s_add_u32 s72, s22, 0x60f00
	s_addc_u32 s73, s90, 0
	s_add_u32 s100, s22, 0x40f00
	s_addc_u32 s101, s90, 0
	global_load_dwordx4 v[12:15], v201, s[100:101] nt
	s_setprio 1
	s_waitcnt lgkmcnt(1)
	v_mfma_f32_16x16x32_f16 v[76:79], v[226:229], v[202:205], v[76:79]
	v_mfma_f32_16x16x32_f16 v[234:237], v[226:229], v[206:209], v[234:237]
	v_mfma_f32_16x16x32_f16 v[158:161], v[226:229], v[210:213], v[158:161]
	v_mfma_f32_16x16x32_f16 v[166:169], v[226:229], v[214:217], v[166:169]
	v_mfma_f32_16x16x32_f16 v[178:181], v[238:241], v[202:205], v[178:181]
	v_mfma_f32_16x16x32_f16 v[182:185], v[238:241], v[206:209], v[182:185]
	v_mfma_f32_16x16x32_f16 v[190:193], v[238:241], v[210:213], v[190:193]
	v_mfma_f32_16x16x32_f16 v[186:189], v[238:241], v[214:217], v[186:189]
	s_setprio 0
	ds_read_b128 v[202:205], v128
	ds_read_b128 v[206:209], v128 offset:2048
	ds_read_b128 v[210:213], v128 offset:4096
	ds_read_b128 v[214:217], v128 offset:6144
	ds_read_b128 v[226:229], v130
	ds_read_b128 v[238:241], v130 offset:2048
	v_cvt_pk_f16_f32 v23, v22, v23
	v_cvt_pk_f16_f32 v22, v20, v21
	ds_write_b64 v100, v[22:23] offset:49152
	s_add_u32 s72, s22, 0x80f00
	s_addc_u32 s73, s90, 0
	s_add_u32 s100, s22, 0x60f00
	s_addc_u32 s101, s90, 0
	global_load_dwordx4 v[16:19], v201, s[100:101] nt
	s_setprio 1
	s_waitcnt lgkmcnt(1)
	v_mfma_f32_16x16x32_f16 v[80:83], v[226:229], v[202:205], v[80:83]
	v_mfma_f32_16x16x32_f16 v[104:107], v[226:229], v[210:213], v[104:107]
	v_mfma_f32_16x16x32_f16 v[108:111], v[238:241], v[202:205], v[108:111]
	v_mfma_f32_16x16x32_f16 v[112:115], v[238:241], v[206:209], v[112:115]
	v_mfma_f32_16x16x32_f16 v[116:119], v[238:241], v[210:213], v[116:119]
	v_mfma_f32_16x16x32_f16 v[230:233], v[226:229], v[206:209], v[230:233]
	v_mfma_f32_16x16x32_f16 v[218:221], v[226:229], v[214:217], v[218:221]
	v_mfma_f32_16x16x32_f16 v[222:225], v[238:241], v[214:217], v[222:225]
	s_setprio 0
	ds_read_b128 v[226:229], v130 offset:4096
	ds_read_b128 v[238:241], v130 offset:6144
	v_cvt_pk_f16_f32 v27, v26, v27
	v_cvt_pk_f16_f32 v26, v24, v25
	ds_write_b64 v100, v[26:27] offset:53248
	s_add_u32 s72, s22, 0xa0f00
	s_addc_u32 s73, s90, 0
	s_add_u32 s100, s22, 0x80f00
	s_addc_u32 s101, s90, 0
	global_load_dwordx4 v[20:23], v201, s[100:101] nt
	s_setprio 1
	s_waitcnt lgkmcnt(1)
	v_mfma_f32_16x16x32_f16 v[68:71], v[226:229], v[202:205], v[68:71]
	v_mfma_f32_16x16x32_f16 v[64:67], v[226:229], v[206:209], v[64:67]
	v_mfma_f32_16x16x32_f16 v[84:87], v[226:229], v[210:213], v[84:87]
	v_mfma_f32_16x16x32_f16 v[120:123], v[226:229], v[214:217], v[120:123]
	v_mfma_f32_16x16x32_f16 v[124:127], v[238:241], v[202:205], v[124:127]
	v_mfma_f32_16x16x32_f16 v[134:137], v[238:241], v[214:217], v[134:137]
	v_mfma_f32_16x16x32_f16 v[138:141], v[238:241], v[206:209], v[138:141]
	v_mfma_f32_16x16x32_f16 v[142:145], v[238:241], v[210:213], v[142:145]
	s_setprio 0
	ds_read_b128 v[226:229], v130 offset:8192
	ds_read_b128 v[238:241], v130 offset:10240
	v_cvt_pk_f16_f32 v31, v30, v31
	v_cvt_pk_f16_f32 v30, v28, v29
	ds_write_b64 v100, v[30:31] offset:57344
	s_add_u32 s72, s22, 0xc0f00
	s_addc_u32 s73, s90, 0
	s_add_u32 s100, s22, 0xa0f00
	s_addc_u32 s101, s90, 0
	global_load_dwordx4 v[24:27], v201, s[100:101] nt
	s_setprio 1
	s_waitcnt lgkmcnt(1)
	v_mfma_f32_16x16x32_f16 v[72:75], v[226:229], v[202:205], v[72:75]
	v_mfma_f32_16x16x32_f16 v[88:91], v[226:229], v[206:209], v[88:91]
	v_mfma_f32_16x16x32_f16 v[146:149], v[226:229], v[214:217], v[146:149]
	v_mfma_f32_16x16x32_f16 v[170:173], v[226:229], v[210:213], v[170:173]
	v_mfma_f32_16x16x32_f16 v[150:153], v[238:241], v[202:205], v[150:153]
	v_mfma_f32_16x16x32_f16 v[162:165], v[238:241], v[206:209], v[162:165]
	v_mfma_f32_16x16x32_f16 v[174:177], v[238:241], v[210:213], v[174:177]
	v_mfma_f32_16x16x32_f16 v[154:157], v[238:241], v[214:217], v[154:157]
	s_setprio 0
	ds_read_b128 v[226:229], v130 offset:12288
	ds_read_b128 v[238:241], v130 offset:14336
	v_cvt_pk_f16_f32 v35, v34, v35
	v_cvt_pk_f16_f32 v34, v32, v33
	ds_write_b64 v100, v[34:35] offset:61440
	s_add_u32 s72, s22, 0xe0f00
	s_addc_u32 s73, s90, 0
	s_add_u32 s100, s22, 0xc0f00
	s_addc_u32 s101, s90, 0
	global_load_dwordx4 v[28:31], v201, s[100:101] nt
	s_add_u32 s100, s22, 0xe0f00
	s_addc_u32 s101, s90, 0
	global_load_dwordx4 v[32:35], v201, s[100:101] nt
	s_setprio 1
	s_waitcnt lgkmcnt(1)
	v_mfma_f32_16x16x32_f16 v[76:79], v[226:229], v[202:205], v[76:79]
	v_mfma_f32_16x16x32_f16 v[234:237], v[226:229], v[206:209], v[234:237]
	v_mfma_f32_16x16x32_f16 v[158:161], v[226:229], v[210:213], v[158:161]
	v_mfma_f32_16x16x32_f16 v[166:169], v[226:229], v[214:217], v[166:169]
	v_mfma_f32_16x16x32_f16 v[178:181], v[238:241], v[202:205], v[178:181]
	v_mfma_f32_16x16x32_f16 v[182:185], v[238:241], v[206:209], v[182:185]
	v_mfma_f32_16x16x32_f16 v[190:193], v[238:241], v[210:213], v[190:193]
	v_mfma_f32_16x16x32_f16 v[186:189], v[238:241], v[214:217], v[186:189]
	s_setprio 0
	s_waitcnt vmcnt(6)
	s_waitcnt lgkmcnt(0)
	s_barrier
	ds_read_b128 v[202:205], v131 offset:32768
	ds_read_b128 v[206:209], v131 offset:34816
	ds_read_b128 v[210:213], v131 offset:36864
	ds_read_b128 v[214:217], v131 offset:38912
	ds_read_b128 v[226:229], v129 offset:32768
	ds_read_b128 v[238:241], v129 offset:34816
	v_lshl_add_u64 v[198:199], s[54:55], 0, v[196:197]
	v_readfirstlane_b32 s64, v94
	s_mov_b32 m0, s64
	v_cvt_pk_f16_f32 v11, v10, v11
	global_load_lds_dwordx4 v[198:199], off
	v_cvt_pk_f16_f32 v10, v8, v9
	ds_write_b64 v100, v[10:11]
	s_setprio 1
	s_waitcnt lgkmcnt(1)
	v_mfma_f32_16x16x32_f16 v[8:11], v[226:229], v[202:205], v[80:83]
	v_mfma_f32_16x16x32_f16 v[80:83], v[226:229], v[206:209], v[230:233]
	v_mfma_f32_16x16x32_f16 v[92:95], v[226:229], v[210:213], v[104:107]
	v_mfma_f32_16x16x32_f16 v[104:107], v[226:229], v[214:217], v[218:221]
	v_mfma_f32_16x16x32_f16 v[108:111], v[238:241], v[202:205], v[108:111]
	v_mfma_f32_16x16x32_f16 v[112:115], v[238:241], v[206:209], v[112:115]
	v_mfma_f32_16x16x32_f16 v[116:119], v[238:241], v[210:213], v[116:119]
	v_mfma_f32_16x16x32_f16 v[218:221], v[238:241], v[214:217], v[222:225]
	s_setprio 0
	s_nop 1
	ds_read_b128 v[222:225], v129 offset:36864
	ds_read_b128 v[226:229], v129 offset:38912
	v_readfirstlane_b32 s64, v99
	v_lshl_add_u64 v[96:97], v[198:199], 0, s[58:59]
	s_mov_b32 m0, s64
	v_cvt_pk_f16_f32 v43, v42, v43
	global_load_lds_dwordx4 v[96:97], off
	v_cvt_pk_f16_f32 v42, v40, v41
	ds_write_b64 v100, v[42:43] offset:4096
	s_setprio 1
	s_waitcnt lgkmcnt(1)
	v_mfma_f32_16x16x32_f16 v[40:43], v[222:225], v[202:205], v[68:71]
	v_mfma_f32_16x16x32_f16 v[64:67], v[222:225], v[206:209], v[64:67]
	v_mfma_f32_16x16x32_f16 v[68:71], v[222:225], v[210:213], v[84:87]
	v_mfma_f32_16x16x32_f16 v[84:87], v[222:225], v[214:217], v[120:123]
	v_mfma_f32_16x16x32_f16 v[96:99], v[226:229], v[202:205], v[124:127]
	v_mfma_f32_16x16x32_f16 v[120:123], v[226:229], v[206:209], v[138:141]
	v_mfma_f32_16x16x32_f16 v[124:127], v[226:229], v[210:213], v[142:145]
	v_mfma_f32_16x16x32_f16 v[134:137], v[226:229], v[214:217], v[134:137]
	s_setprio 0
	ds_read_b128 v[138:141], v129 offset:40960
	ds_read_b128 v[142:145], v129 offset:43008
	v_readfirstlane_b32 s64, v101
	v_lshl_add_u64 v[222:223], v[198:199], 0, s[60:61]
	s_mov_b32 m0, s64
	v_cvt_pk_f16_f32 v47, v46, v47
	global_load_lds_dwordx4 v[222:223], off
	v_cvt_pk_f16_f32 v46, v44, v45
	ds_write_b64 v100, v[46:47] offset:8192
	s_setprio 1
	s_waitcnt lgkmcnt(1)
	v_mfma_f32_16x16x32_f16 v[44:47], v[138:141], v[202:205], v[72:75]
	v_mfma_f32_16x16x32_f16 v[72:75], v[138:141], v[206:209], v[88:91]
	v_mfma_f32_16x16x32_f16 v[88:91], v[138:141], v[210:213], v[170:173]
	v_mfma_f32_16x16x32_f16 v[138:141], v[138:141], v[214:217], v[146:149]
	v_mfma_f32_16x16x32_f16 v[146:149], v[142:145], v[202:205], v[150:153]
	v_mfma_f32_16x16x32_f16 v[150:153], v[142:145], v[206:209], v[162:165]
	v_mfma_f32_16x16x32_f16 v[162:165], v[142:145], v[210:213], v[174:177]
	v_mfma_f32_16x16x32_f16 v[142:145], v[142:145], v[214:217], v[154:157]
	s_setprio 0
	s_nop 1
	ds_read_b128 v[154:157], v129 offset:45056
	ds_read_b128 v[170:173], v129 offset:47104
	v_readfirstlane_b32 s64, v102
	v_lshl_add_u64 v[174:175], v[198:199], 0, s[62:63]
	s_mov_b32 m0, s64
	v_cvt_pk_f16_f32 v51, v50, v51
	global_load_lds_dwordx4 v[174:175], off
	v_cvt_pk_f16_f32 v50, v48, v49
	ds_write_b64 v100, v[50:51] offset:12288
	s_setprio 1
	s_waitcnt lgkmcnt(1)
	v_mfma_f32_16x16x32_f16 v[48:51], v[154:157], v[202:205], v[76:79]
	v_mfma_f32_16x16x32_f16 v[76:79], v[154:157], v[206:209], v[234:237]
	v_mfma_f32_16x16x32_f16 v[158:161], v[154:157], v[210:213], v[158:161]
	v_mfma_f32_16x16x32_f16 v[154:157], v[154:157], v[214:217], v[166:169]
	v_mfma_f32_16x16x32_f16 v[166:169], v[170:173], v[202:205], v[178:181]
	v_mfma_f32_16x16x32_f16 v[174:177], v[170:173], v[206:209], v[182:185]
	v_mfma_f32_16x16x32_f16 v[178:181], v[170:173], v[210:213], v[190:193]
	v_mfma_f32_16x16x32_f16 v[170:173], v[170:173], v[214:217], v[186:189]
	s_setprio 0
	ds_read_b128 v[182:185], v128 offset:32768
	s_nop 0
	ds_read_b128 v[186:189], v128 offset:34816
	ds_read_b128 v[190:193], v128 offset:36864
	ds_read_b128 v[202:205], v128 offset:38912
	ds_read_b128 v[206:209], v130 offset:32768
	ds_read_b128 v[210:213], v130 offset:34816
	v_cvt_pk_f16_f32 v55, v54, v55
	v_cvt_pk_f16_f32 v54, v52, v53
	ds_write_b64 v100, v[54:55] offset:16384
	s_setprio 1
	s_waitcnt lgkmcnt(1)
	v_mfma_f32_16x16x32_f16 v[8:11], v[206:209], v[182:185], v[8:11]
	v_mfma_f32_16x16x32_f16 v[52:55], v[206:209], v[186:189], v[80:83]
	v_mfma_f32_16x16x32_f16 v[80:83], v[206:209], v[190:193], v[92:95]
	v_mfma_f32_16x16x32_f16 v[92:95], v[206:209], v[202:205], v[104:107]
	v_mfma_f32_16x16x32_f16 v[102:105], v[210:213], v[182:185], v[108:111]
	v_mfma_f32_16x16x32_f16 v[106:109], v[210:213], v[186:189], v[112:115]
	v_mfma_f32_16x16x32_f16 v[110:113], v[210:213], v[190:193], v[116:119]
	v_mfma_f32_16x16x32_f16 v[114:117], v[210:213], v[202:205], v[218:221]
	s_setprio 0
	ds_read_b128 v[206:209], v130 offset:36864
	ds_read_b128 v[210:213], v130 offset:38912
	v_cvt_pk_f16_f32 v59, v58, v59
	v_cvt_pk_f16_f32 v58, v56, v57
	ds_write_b64 v100, v[58:59] offset:20480
	s_setprio 1
	s_waitcnt lgkmcnt(1)
	v_mfma_f32_16x16x32_f16 v[40:43], v[206:209], v[182:185], v[40:43]
	v_mfma_f32_16x16x32_f16 v[56:59], v[206:209], v[186:189], v[64:67]
	v_mfma_f32_16x16x32_f16 v[64:67], v[206:209], v[190:193], v[68:71]
	v_mfma_f32_16x16x32_f16 v[68:71], v[206:209], v[202:205], v[84:87]
	v_mfma_f32_16x16x32_f16 v[84:87], v[210:213], v[182:185], v[96:99]
	v_mfma_f32_16x16x32_f16 v[96:99], v[210:213], v[186:189], v[120:123]
	v_mfma_f32_16x16x32_f16 v[118:121], v[210:213], v[190:193], v[124:127]
	v_mfma_f32_16x16x32_f16 v[122:125], v[210:213], v[202:205], v[134:137]
	s_setprio 0
	s_nop 1
	ds_read_b128 v[134:137], v130 offset:40960
	ds_read_b128 v[206:209], v130 offset:43008
	v_cvt_pk_f16_f32 v63, v62, v63
	v_cvt_pk_f16_f32 v62, v60, v61
	ds_write_b64 v100, v[62:63] offset:24576
	s_setprio 1
	s_waitcnt lgkmcnt(1)
	v_mfma_f32_16x16x32_f16 v[44:47], v[134:137], v[182:185], v[44:47]
	v_mfma_f32_16x16x32_f16 v[60:63], v[134:137], v[186:189], v[72:75]
	v_mfma_f32_16x16x32_f16 v[72:75], v[134:137], v[190:193], v[88:91]
	v_mfma_f32_16x16x32_f16 v[88:91], v[134:137], v[202:205], v[138:141]
	v_mfma_f32_16x16x32_f16 v[134:137], v[206:209], v[182:185], v[146:149]
	v_mfma_f32_16x16x32_f16 v[146:149], v[206:209], v[190:193], v[162:165]
	v_mfma_f32_16x16x32_f16 v[138:141], v[206:209], v[186:189], v[150:153]
	v_mfma_f32_16x16x32_f16 v[142:145], v[206:209], v[202:205], v[142:145]
	s_setprio 0
	s_nop 0
	ds_read_b128 v[150:153], v130 offset:45056
	ds_read_b128 v[162:165], v130 offset:47104
	v_cvt_pk_f16_f32 v39, v38, v39
	v_cvt_pk_f16_f32 v38, v36, v37
	ds_write_b64 v100, v[38:39] offset:28672
	s_setprio 1
	s_waitcnt lgkmcnt(1)
	v_mfma_f32_16x16x32_f16 v[36:39], v[150:153], v[182:185], v[48:51]
	v_mfma_f32_16x16x32_f16 v[48:51], v[150:153], v[186:189], v[76:79]
	v_mfma_f32_16x16x32_f16 v[76:79], v[150:153], v[190:193], v[158:161]
	v_mfma_f32_16x16x32_f16 v[150:153], v[150:153], v[202:205], v[154:157]
	v_mfma_f32_16x16x32_f16 v[154:157], v[162:165], v[182:185], v[166:169]
	v_mfma_f32_16x16x32_f16 v[158:161], v[162:165], v[186:189], v[174:177]
	v_mfma_f32_16x16x32_f16 v[166:169], v[162:165], v[190:193], v[178:181]
	v_mfma_f32_16x16x32_f16 v[162:165], v[162:165], v[202:205], v[170:173]
	s_setprio 0
	s_waitcnt vmcnt(0)
	s_waitcnt lgkmcnt(0)
	s_barrier
	s_nop 0
	ds_read_b128 v[170:173], v131
	ds_read_b128 v[174:177], v131 offset:2048
	ds_read_b128 v[178:181], v131 offset:4096
	ds_read_b128 v[182:185], v131 offset:6144
	ds_read_b128 v[186:189], v129
	ds_read_b128 v[190:193], v129 offset:2048
	v_lshl_add_u64 v[126:127], s[56:57], 0, v[196:197]
	s_mov_b32 m0, s0
	v_cvt_pk_f16_f32 v3, v2, v3
	global_load_lds_dwordx4 v[126:127], off
	v_cvt_pk_f16_f32 v2, v0, v1
	ds_write_b64 v100, v[2:3] offset:32768
	s_setprio 1
	s_waitcnt lgkmcnt(1)
	v_mfma_f32_16x16x32_f16 v[0:3], v[186:189], v[170:173], v[8:11]
	v_mfma_f32_16x16x32_f16 v[8:11], v[186:189], v[174:177], v[52:55]
	v_mfma_f32_16x16x32_f16 v[52:55], v[186:189], v[178:181], v[80:83]
	v_mfma_f32_16x16x32_f16 v[80:83], v[186:189], v[182:185], v[92:95]
	v_mfma_f32_16x16x32_f16 v[92:95], v[190:193], v[170:173], v[102:105]
	v_mfma_f32_16x16x32_f16 v[102:105], v[190:193], v[174:177], v[106:109]
	v_mfma_f32_16x16x32_f16 v[106:109], v[190:193], v[178:181], v[110:113]
	v_mfma_f32_16x16x32_f16 v[110:113], v[190:193], v[182:185], v[114:117]
	s_setprio 0
	s_nop 1
	ds_read_b128 v[114:117], v129 offset:4096
	ds_read_b128 v[186:189], v129 offset:6144
	s_mov_b32 m0, s1
	v_lshl_add_u64 v[190:191], v[126:127], 0, s[58:59]
	global_load_lds_dwordx4 v[190:191], off
	v_cvt_pk_f16_f32 v7, v6, v7
	v_cvt_pk_f16_f32 v6, v4, v5
	ds_write_b64 v100, v[6:7] offset:36864
	s_setprio 1
	s_waitcnt lgkmcnt(1)
	v_mfma_f32_16x16x32_f16 v[190:193], v[114:117], v[170:173], v[40:43]
	v_mfma_f32_16x16x32_f16 v[56:59], v[114:117], v[174:177], v[56:59]
	v_mfma_f32_16x16x32_f16 v[64:67], v[114:117], v[178:181], v[64:67]
	v_mfma_f32_16x16x32_f16 v[68:71], v[114:117], v[182:185], v[68:71]
	v_mfma_f32_16x16x32_f16 v[84:87], v[186:189], v[170:173], v[84:87]
	v_mfma_f32_16x16x32_f16 v[96:99], v[186:189], v[174:177], v[96:99]
	v_mfma_f32_16x16x32_f16 v[114:117], v[186:189], v[178:181], v[118:121]
	v_mfma_f32_16x16x32_f16 v[118:121], v[186:189], v[182:185], v[122:125]
	s_setprio 0
	ds_read_b128 v[4:7], v129 offset:8192
	ds_read_b128 v[40:43], v129 offset:10240
	s_mov_b32 m0, s70
	v_lshl_add_u64 v[122:123], v[126:127], 0, s[60:61]
	global_load_lds_dwordx4 v[122:123], off
	v_cvt_pk_f16_f32 v15, v14, v15
	v_cvt_pk_f16_f32 v14, v12, v13
	ds_write_b64 v100, v[14:15] offset:40960
	s_setprio 1
	s_waitcnt lgkmcnt(1)
	v_mfma_f32_16x16x32_f16 v[122:125], v[4:7], v[170:173], v[44:47]
	v_mfma_f32_16x16x32_f16 v[88:91], v[4:7], v[182:185], v[88:91]
	v_mfma_f32_16x16x32_f16 v[134:137], v[40:43], v[170:173], v[134:137]
	v_mfma_f32_16x16x32_f16 v[146:149], v[40:43], v[178:181], v[146:149]
	v_mfma_f32_16x16x32_f16 v[186:189], v[4:7], v[174:177], v[60:63]
	v_mfma_f32_16x16x32_f16 v[202:205], v[4:7], v[178:181], v[72:75]
	v_mfma_f32_16x16x32_f16 v[138:141], v[40:43], v[174:177], v[138:141]
	v_mfma_f32_16x16x32_f16 v[142:145], v[40:43], v[182:185], v[142:145]
	s_setprio 0
	ds_read_b128 v[4:7], v129 offset:12288
	ds_read_b128 v[12:15], v129 offset:14336
	s_mov_b32 m0, s71
	v_lshl_add_u64 v[40:41], v[126:127], 0, s[62:63]
	global_load_lds_dwordx4 v[40:41], off
	v_cvt_pk_f16_f32 v19, v18, v19
	v_cvt_pk_f16_f32 v18, v16, v17
	ds_write_b64 v100, v[18:19] offset:45056
	s_setprio 1
	s_waitcnt lgkmcnt(1)
	v_mfma_f32_16x16x32_f16 v[206:209], v[4:7], v[170:173], v[36:39]
	v_mfma_f32_16x16x32_f16 v[210:213], v[4:7], v[174:177], v[48:51]
	v_mfma_f32_16x16x32_f16 v[214:217], v[4:7], v[178:181], v[76:79]
	v_mfma_f32_16x16x32_f16 v[150:153], v[4:7], v[182:185], v[150:153]
	v_mfma_f32_16x16x32_f16 v[154:157], v[12:15], v[170:173], v[154:157]
	v_mfma_f32_16x16x32_f16 v[158:161], v[12:15], v[174:177], v[158:161]
	v_mfma_f32_16x16x32_f16 v[166:169], v[12:15], v[178:181], v[166:169]
	v_mfma_f32_16x16x32_f16 v[162:165], v[12:15], v[182:185], v[162:165]
	s_setprio 0
	ds_read_b128 v[170:173], v128
	ds_read_b128 v[174:177], v128 offset:2048
	ds_read_b128 v[178:181], v128 offset:4096
	ds_read_b128 v[182:185], v128 offset:6144
	ds_read_b128 v[12:15], v130
	ds_read_b128 v[40:43], v130 offset:2048
	v_cvt_pk_f16_f32 v5, v22, v23
	v_cvt_pk_f16_f32 v4, v20, v21
	ds_write_b64 v100, v[4:5] offset:49152
	s_setprio 1
	s_waitcnt lgkmcnt(1)
	v_mfma_f32_16x16x32_f16 v[0:3], v[12:15], v[170:173], v[0:3]
	v_mfma_f32_16x16x32_f16 v[4:7], v[12:15], v[174:177], v[8:11]
	v_mfma_f32_16x16x32_f16 v[8:11], v[12:15], v[178:181], v[52:55]
	v_mfma_f32_16x16x32_f16 v[12:15], v[12:15], v[182:185], v[80:83]
	v_mfma_f32_16x16x32_f16 v[16:19], v[40:43], v[170:173], v[92:95]
	v_mfma_f32_16x16x32_f16 v[20:23], v[40:43], v[174:177], v[102:105]
	v_mfma_f32_16x16x32_f16 v[36:39], v[40:43], v[178:181], v[106:109]
	v_mfma_f32_16x16x32_f16 v[40:43], v[40:43], v[182:185], v[110:113]
	s_setprio 0
	ds_read_b128 v[52:55], v130 offset:4096
	ds_read_b128 v[72:75], v130 offset:6144
	v_cvt_pk_f16_f32 v27, v26, v27
	v_cvt_pk_f16_f32 v26, v24, v25
	ds_write_b64 v100, v[26:27] offset:53248
	s_setprio 1
	s_waitcnt lgkmcnt(1)
	v_mfma_f32_16x16x32_f16 v[24:27], v[52:55], v[170:173], v[190:193]
	v_mfma_f32_16x16x32_f16 v[44:47], v[52:55], v[174:177], v[56:59]
	v_mfma_f32_16x16x32_f16 v[48:51], v[52:55], v[178:181], v[64:67]
	v_mfma_f32_16x16x32_f16 v[52:55], v[52:55], v[182:185], v[68:71]
	v_mfma_f32_16x16x32_f16 v[56:59], v[72:75], v[170:173], v[84:87]
	v_mfma_f32_16x16x32_f16 v[60:63], v[72:75], v[174:177], v[96:99]
	v_mfma_f32_16x16x32_f16 v[64:67], v[72:75], v[178:181], v[114:117]
	v_mfma_f32_16x16x32_f16 v[68:71], v[72:75], v[182:185], v[118:121]
	s_setprio 0
	ds_read_b128 v[80:83], v130 offset:8192
	ds_read_b128 v[96:99], v130 offset:10240
	v_cvt_pk_f16_f32 v31, v30, v31
	v_cvt_pk_f16_f32 v30, v28, v29
	ds_write_b64 v100, v[30:31] offset:57344
	s_setprio 1
	s_waitcnt lgkmcnt(1)
	v_mfma_f32_16x16x32_f16 v[28:31], v[80:83], v[170:173], v[122:125]
	v_mfma_f32_16x16x32_f16 v[72:75], v[80:83], v[174:177], v[186:189]
	v_mfma_f32_16x16x32_f16 v[76:79], v[80:83], v[178:181], v[202:205]
	v_mfma_f32_16x16x32_f16 v[80:83], v[80:83], v[182:185], v[88:91]
	v_mfma_f32_16x16x32_f16 v[84:87], v[96:99], v[170:173], v[134:137]
	v_mfma_f32_16x16x32_f16 v[88:91], v[96:99], v[174:177], v[138:141]
	v_mfma_f32_16x16x32_f16 v[92:95], v[96:99], v[178:181], v[146:149]
	v_mfma_f32_16x16x32_f16 v[96:99], v[96:99], v[182:185], v[142:145]
	s_setprio 0
	ds_read_b128 v[108:111], v130 offset:12288
	ds_read_b128 v[124:127], v130 offset:14336
	v_cvt_pk_f16_f32 v35, v34, v35
	v_cvt_pk_f16_f32 v34, v32, v33
	ds_write_b64 v100, v[34:35] offset:61440
	s_setprio 1
	s_waitcnt lgkmcnt(1)
	v_mfma_f32_16x16x32_f16 v[32:35], v[108:111], v[170:173], v[206:209]
	v_mfma_f32_16x16x32_f16 v[100:103], v[108:111], v[174:177], v[210:213]
	v_mfma_f32_16x16x32_f16 v[104:107], v[108:111], v[178:181], v[214:217]
	v_mfma_f32_16x16x32_f16 v[108:111], v[108:111], v[182:185], v[150:153]
	v_mfma_f32_16x16x32_f16 v[112:115], v[124:127], v[170:173], v[154:157]
	v_mfma_f32_16x16x32_f16 v[116:119], v[124:127], v[174:177], v[158:161]
	v_mfma_f32_16x16x32_f16 v[120:123], v[124:127], v[178:181], v[166:169]
	v_mfma_f32_16x16x32_f16 v[124:127], v[124:127], v[182:185], v[162:165]
	s_setprio 0
	s_waitcnt vmcnt(0)
	s_waitcnt lgkmcnt(0)
	s_barrier
	ds_read_b128 v[134:137], v131 offset:32768
	ds_read_b128 v[138:141], v131 offset:34816
	ds_read_b128 v[142:145], v131 offset:36864
	ds_read_b128 v[148:151], v131 offset:38912
	ds_read_b128 v[152:155], v129 offset:32768
	ds_read_b128 v[156:159], v129 offset:34816
	s_setprio 1
	s_waitcnt lgkmcnt(0)
	v_mfma_f32_16x16x32_f16 v[0:3], v[152:155], v[134:137], v[0:3]
	v_mfma_f32_16x16x32_f16 v[4:7], v[152:155], v[138:141], v[4:7]
	v_mfma_f32_16x16x32_f16 v[8:11], v[152:155], v[142:145], v[8:11]
	v_mfma_f32_16x16x32_f16 v[12:15], v[152:155], v[148:151], v[12:15]
	v_mfma_f32_16x16x32_f16 v[16:19], v[156:159], v[134:137], v[16:19]
	v_mfma_f32_16x16x32_f16 v[20:23], v[156:159], v[138:141], v[20:23]
	v_mfma_f32_16x16x32_f16 v[36:39], v[156:159], v[142:145], v[36:39]
	v_mfma_f32_16x16x32_f16 v[40:43], v[156:159], v[148:151], v[40:43]
	s_setprio 0
	ds_read_b128 v[152:155], v129 offset:36864
	ds_read_b128 v[156:159], v129 offset:38912
	v_and_b32_e32 v250, 0x7ffffc00, v194
	v_lshl_add_u64 v[252:253], s[10:11], 0, v[196:197]
	v_readfirstlane_b32 s32, v250
	s_nop 0
	s_mov_b32 m0, s32
	s_nop 0
	global_load_lds_dwordx4 v[252:253], off
	v_mov_b32_e32 v146, 0
	v_and_b32_e32 v251, 0xfffffff, v132
	v_cmp_gt_u32_e32 vcc, s82, v251
	v_mov_b32_e32 v132, 0
	v_mov_b32_e32 v133, 0
	s_and_saveexec_b64 s[0:1], vcc
	s_cbranch_execz .LBB1_7
	s_and_b32 s64, s78, 0x7ffffc00
	s_or_b32 s64, s64, s33
	v_or_b32_e32 v132, s64, v251
	v_mov_b32_e32 v133, v195
	v_lshl_add_u64 v[132:133], v[132:133], 2, s[12:13]
	global_load_dword v133, v[132:133], off
	v_or_b32_e32 v132, s33, v251
	v_lshlrev_b32_e32 v132, 2, v132
	global_load_dword v146, v132, s[16:17]
	s_nop 0
	global_load_dword v132, v132, s[14:15]
